# speedup vs baseline: 1.0483x; 1.0483x over previous
.LBB0_3:
	s_mov_b32 s8, 0xbffff
	v_cmp_lt_u32_e32 vcc, s8, v2
	s_and_saveexec_b64 s[8:9], vcc
	s_xor_b64 s[12:13], exec, s[8:9]
	s_cbranch_execz .LBB0_15
	s_load_dwordx4 s[8:11], s[0:1], 0x48
	s_mov_b32 s14, 0xeffff
	v_cmp_lt_u32_e32 vcc, s14, v2
	s_and_saveexec_b64 s[14:15], vcc
	s_xor_b64 s[14:15], exec, s[14:15]
	s_cbranch_execz .LBB0_8
	s_mov_b32 s16, 0x153010
	v_cmp_gt_u32_e32 vcc, s16, v2
	s_and_saveexec_b64 s[16:17], vcc
	s_cbranch_execz .LBB0_7
	v_mov_b32_e32 v0, 0xff100000
	v_lshl_add_u32 v0, v2, 4, v0
	v_mov_b32_e32 v2, -1
	s_waitcnt lgkmcnt(0)
	s_and_b32 s21, s11, 0xffff
	s_mov_b32 s23, 0x20000
	s_mov_b32 s22, 0x6b0100
	s_mov_b32 s20, s10
	v_mov_b32_e32 v3, v2
	v_mov_b32_e32 v4, v2
	v_mov_b32_e32 v5, v2
	buffer_store_dwordx4 v[2:5], v0, s[20:23], 0 offen sc1
	v_cmp_gt_u32_e32 vcc, 0x80000, v0
	v_add_u32_e32 v0, 0x630100, v0
	s_and_b64 exec, exec, vcc
	s_cbranch_execz .LBB0_7
	buffer_store_dwordx4 v[2:5], v0, s[20:23], 0 offen sc1

.LBB3_25:
	s_waitcnt vmcnt(32)
	v_mul_f32_e32 v7, 0xbfb8aa3b, v7
	v_add_f32_e32 v8, v8, v8
	v_exp_f32_e32 v7, v7
	v_mul_f32_e32 v8, 0x3fb8aa3b, v8
	v_exp_f32_e32 v8, v8
	v_mul_f32_e32 v6, 0xbfb8aa3b, v6
	v_exp_f32_e32 v13, v6
	v_add_f32_e32 v7, 1.0, v7
	v_rcp_f32_e32 v6, v7
	v_add_f32_e32 v7, 1.0, v8
	v_rcp_f32_e32 v8, v7
	v_add_f32_e32 v7, 1.0, v13
	v_rcp_f32_e32 v7, v7
	v_mov_b32_e32 v16, 0
	v_fma_f32 v17, v8, -2.0, 1.0
	s_add_i32 s2, 0, 0x20000
	v_pk_mul_f32 v[6:7], v[6:7], v[16:17]
	v_lshl_add_u32 v15, v1, 7, s2
	v_add_f32_e32 v172, v6, v7
	v_add_f32_e32 v7, v172, v172
	v_mul_f32_e32 v7, 0x3fb8aa3b, v7
	v_mul_f32_e32 v6, 0xbfb8aa3b, v9
	v_exp_f32_e32 v7, v7
	v_exp_f32_e32 v6, v6
	v_lshl_add_u32 v8, v14, 1, v15
	s_xor_b64 s[6:7], s[4:5], -1
	v_add_f32_e32 v7, 1.0, v7
	v_add_f32_e32 v6, 1.0, v6
	v_rcp_f32_e32 v7, v7
	v_rcp_f32_e32 v6, v6
	v_cmp_gt_u32_e64 s[4:5], 16, v10
	v_fma_f32 v7, v7, -2.0, 1.0
	v_fma_mixlo_f16 v6, v6, v7, 0
	v_lshlrev_b32_e32 v7, 3, v11
	v_add_u32_e32 v171, v8, v7
	ds_write_b16 v171, v6
	v_lshlrev_b32_e32 v6, 1, v12
	s_and_saveexec_b64 s[12:13], s[4:5]
	s_cbranch_execz .LBB3_33
	s_lshl_b32 s2, s29, 8
	s_lshl_b32 s3, s28, 3
	v_lshl_add_u32 v7, v10, 3, v15
	v_or_b32_e32 v18, s30, v10
	s_add_i32 s2, s3, s2
	ds_read_b64 v[8:9], v7
	v_ashrrev_i32_e32 v19, 31, v18
	s_ashr_i32 s3, s2, 31
	v_lshlrev_b64 v[18:19], 11, v[18:19]
	s_ashr_i32 s23, s22, 31
	s_lshl_b64 s[2:3], s[2:3], 2
	v_lshl_add_u64 v[18:19], s[8:9], 0, v[18:19]
	s_add_u32 s2, s10, s2
	v_lshl_add_u64 v[18:19], s[22:23], 1, v[18:19]
	v_mov_b32_e32 v7, v16
	s_addc_u32 s3, s11, s3
	v_mov_b32_e32 v13, v16
	v_lshl_add_u64 v[18:19], v[18:19], 0, v[6:7]
	s_lshl_b32 s42, s29, 5
	s_add_i32 s42, s42, s28
	s_lshl_b32 s42, s42, 10
	s_add_i32 s42, s42, 0x630100
	v_lshrrev_b32_e32 v240, 1, v1
	v_lshlrev_b32_e32 v240, 8, v240
	v_and_b32_e32 v20, 1, v1
	v_lshl_add_u32 v240, v20, 3, v240
	v_add3_u32 v240, v240, v170, s42
	v_mov_b32_e32 v241, 0
	v_lshl_add_u64 v[240:241], s[8:9], 0, v[240:241]
	v_lshl_add_u64 v[16:17], s[2:3], 0, v[12:13]
	v_cmp_eq_u32_e64 s[2:3], 0, v10
	s_mov_b64 s[16:17], -1
	s_and_b64 vcc, exec, s[6:7]
	s_cbranch_vccz .LBB3_30
	s_waitcnt lgkmcnt(0)
	global_store_dwordx2 v[18:19], v[8:9], off sc1
	global_store_dwordx2 v[240:241], v[8:9], off sc1
	s_and_saveexec_b64 s[16:17], s[2:3]
	s_cbranch_execz .LBB3_29
	v_mov_b32_e32 v7, 1
	global_store_dword v[16:17], v7, off sc1

.LBB3_30:
	s_andn2_b64 vcc, exec, s[16:17]
	s_cbranch_vccnz .LBB3_33
	s_waitcnt lgkmcnt(0)
	global_store_dwordx2 v[18:19], v[8:9], off sc0
	global_store_dwordx2 v[240:241], v[8:9], off sc0
	s_and_b64 exec, exec, s[2:3]
	s_cbranch_execz .LBB3_33
	v_mov_b32_e32 v7, 1
	global_store_dword v[16:17], v7, off sc0
.LBB3_33:
	s_or_b64 exec, exec, s[12:13]
	s_load_dwordx2 s[0:1], s[0:1], 0x30
	s_waitcnt vmcnt(0)
	v_add_u32_e32 v2, s22, v12
	v_or_b32_e32 v2, v2, v14
	v_ashrrev_i32_e32 v3, 31, v2
	v_lshl_add_u64 v[174:175], v[2:3], 4, s[20:21]
	v_and_b32_e32 v2, 48, v0
	s_lshl_b32 s37, s29, 8
	v_lshlrev_b32_e32 v187, 13, v1
	s_lshl_b32 s42, s29, 15
	s_add_i32 s42, s42, 0x630100
	v_lshrrev_b32_e32 v186, 1, v187
	v_add3_u32 v186, v186, v170, s42
	v_lshl_or_b32 v2, v1, 8, v2
	v_lshl_or_b32 v184, v1, 5, s37
	v_add_u32_e32 v1, 0x2000, v187
	v_and_b32_e32 v188, 0xe000, v1
	v_add_u32_e32 v1, 0x4000, v187
	s_ashr_i32 s23, s22, 31
	v_and_b32_e32 v189, 0xe000, v1
	v_add_u32_e32 v1, 0x6000, v187
	s_and_b32 s17, s9, 0xffff
	s_lshl_b64 s[2:3], s[22:23], 1
	v_and_b32_e32 v190, 0xe000, v1
	v_add_u32_e32 v1, 0xa000, v187
	v_and_b32_e32 v0, 31, v0
	v_mov_b32_e32 v177, 0
	s_add_u32 s2, s8, s2
	v_and_b32_e32 v191, 0xe000, v1
	v_add_u32_e32 v1, 0xc000, v187
	s_mov_b32 s16, s8
	v_or_b32_e32 v169, s30, v11
	v_lshlrev_b32_e32 v176, 2, v0
	v_lshlrev_b32_e32 v0, 3, v10
	s_addc_u32 s3, s9, s3
	v_mov_b32_e32 v7, v177
	v_mov_b32_e32 v13, v177
	v_and_b32_e32 v192, 0xe000, v1
	v_add_u32_e32 v1, 0xe000, v187
	s_lshl_b32 s8, s28, 3
	s_mov_b32 s19, 0x20000
	s_mov_b32 s18, 0x6b0100
	v_lshl_add_u64 v[178:179], s[10:11], 0, v[176:177]
	v_add_u32_e32 v185, s30, v10
	s_mov_b32 s36, 1
	v_lshl_add_u64 v[180:181], s[2:3], 0, v[6:7]
	v_lshl_add_u64 v[182:183], s[10:11], 0, v[12:13]
	v_cmp_eq_u32_e64 s[2:3], 0, v10
	v_and_b32_e32 v193, 0xe000, v1
	s_add_i32 s37, s37, s8
	v_xor_b32_e32 v194, 0x8000, v187
	s_mov_b64 s[8:9], 0
	s_mov_b32 s38, 0x186a0
	s_mov_b32 s39, 0x40004000
	s_mov_b32 s40, 0xbb8000
	v_add_u32_e32 v195, v15, v0
	v_mov_b32_e32 v196, 1
	v_mov_b32_e32 v0, v177
	v_mov_b32_e32 v1, v177
	v_mov_b32_e32 v2, v177
	v_mov_b32_e32 v3, v177
	v_mov_b32_e32 v4, v177
	v_mov_b32_e32 v5, v177
	v_mov_b32_e32 v6, v177
	s_waitcnt lgkmcnt(0)
	v_mov_b32_e32 v8, v177
	v_mov_b32_e32 v9, v177
	v_mov_b32_e32 v10, v177
	v_mov_b32_e32 v11, v177
	v_mov_b32_e32 v12, v177
	v_mov_b32_e32 v14, v177
	v_mov_b32_e32 v15, v177
	v_add_u32_e32 v206, 0x80, v169
	v_mov_b32_e32 v207, 0
	v_lshlrev_b64 v[206:207], 14, v[206:207]
	v_lshl_add_u64 v[206:207], v[174:175], 0, v[206:207]
	global_load_dwordx4 v[160:163], v[206:207], off
.Lrec_loop:
	s_add_i32 s10, s36, -1
	s_and_b32 s48, s10, 1
	v_lshl_add_u32 v164, s48, 18, v186
	s_bfe_u32 s48, s10, 0x10001
	s_mul_i32 s48, s48, 0x40004000
	buffer_load_dwordx4 v[16:19], v164, s[16:19], 0 offen sc1
	buffer_load_dwordx4 v[20:23], v164, s[16:19], 0 offen offset:1024 sc1
	buffer_load_dwordx4 v[24:27], v164, s[16:19], 0 offen offset:2048 sc1
	buffer_load_dwordx4 v[28:31], v164, s[16:19], 0 offen offset:3072 sc1
	s_lshl_b32 s41, s36, 7
	s_mov_b32 s43, 0
	s_mov_b32 s45, 15
	s_mov_b32 s46, 0
	s_add_i32 s11, s41, 0x80
	v_add_u32_e32 v206, s11, v169
	v_mov_b32_e32 v207, 0
	v_lshlrev_b64 v[206:207], 14, v[206:207]
	v_lshl_add_u64 v[206:207], v[174:175], 0, v[206:207]
	s_lshl_b32 s11, s36, 16
	s_and_b32 s11, s11, 0x10000
	v_add_u32_e32 v173, s11, v170

.Lrec_check:
	s_bitcmp1_b32 s45, 0
	s_cbranch_scc0 .Lrec_chk0_done
	v_xor_b32_e32 v16, s48, v16
	v_xor_b32_e32 v17, s48, v17
	v_xor_b32_e32 v18, s48, v18
	v_xor_b32_e32 v19, s48, v19
	v_or3_b32 v0, v16, v17, v18
	v_bitop3_b32 v0, v0, s39, v19 bitop3:0xc8
	v_cmp_ne_u32_e32 vcc, 0, v0
	s_cmp_lg_u64 vcc, 0
	s_cbranch_scc1 .Lrec_chk0_dirty
	s_bitset0_b32 s45, 0
	s_branch .Lrec_chk0_done

.Lrec_chk0_done:
	s_bitcmp1_b32 s45, 1
	s_cbranch_scc0 .Lrec_chk1_done
	v_xor_b32_e32 v20, s48, v20
	v_xor_b32_e32 v21, s48, v21
	v_xor_b32_e32 v22, s48, v22
	v_xor_b32_e32 v23, s48, v23
	v_or3_b32 v0, v20, v21, v22
	v_bitop3_b32 v0, v0, s39, v23 bitop3:0xc8
	v_cmp_ne_u32_e32 vcc, 0, v0
	s_cmp_lg_u64 vcc, 0
	s_cbranch_scc1 .Lrec_chk1_dirty
	s_bitset0_b32 s45, 1
	s_branch .Lrec_chk1_done

.Lrec_chk1_done:
	s_bitcmp1_b32 s45, 2
	s_cbranch_scc0 .Lrec_chk2_done
	v_xor_b32_e32 v24, s48, v24
	v_xor_b32_e32 v25, s48, v25
	v_xor_b32_e32 v26, s48, v26
	v_xor_b32_e32 v27, s48, v27
	v_or3_b32 v0, v24, v25, v26
	v_bitop3_b32 v0, v0, s39, v27 bitop3:0xc8
	v_cmp_ne_u32_e32 vcc, 0, v0
	s_cmp_lg_u64 vcc, 0
	s_cbranch_scc1 .Lrec_chk2_dirty
	s_bitset0_b32 s45, 2
	s_branch .Lrec_chk2_done

.Lrec_chk2_done:
	s_bitcmp1_b32 s45, 3
	s_cbranch_scc0 .Lrec_chk3_done
	v_xor_b32_e32 v28, s48, v28
	v_xor_b32_e32 v29, s48, v29
	v_xor_b32_e32 v30, s48, v30
	v_xor_b32_e32 v31, s48, v31
	v_or3_b32 v0, v28, v29, v30
	v_bitop3_b32 v0, v0, s39, v31 bitop3:0xc8
	v_cmp_ne_u32_e32 vcc, 0, v0
	s_cmp_lg_u64 vcc, 0
	s_cbranch_scc1 .Lrec_chk3_dirty
	s_bitset0_b32 s45, 3
	s_branch .Lrec_chk3_done

.Lrec_ldone:
	v_add_u32_e32 v197, v173, v188
	ds_write_b128 v197, v[198:201] offset:1024
	v_add_u32_e32 v197, v173, v189
	ds_write_b128 v197, v[202:205] offset:2048
	v_add_u32_e32 v197, v173, v190
	ds_write_b128 v197, v[212:215] offset:3072
	v_add_u32_e32 v197, v173, v194
	ds_write_b128 v197, v[216:219] offset:4096
	v_add_u32_e32 v197, v173, v191
	ds_write_b128 v197, v[220:223] offset:5120
	v_add_u32_e32 v197, v173, v192
	ds_write_b128 v197, v[224:227] offset:6144
	v_add_u32_e32 v197, v173, v193
	ds_write_b128 v197, v[228:231] offset:7168
	v_add_u32_e32 v173, v173, v187
	s_waitcnt lgkmcnt(0)
	s_barrier
	ds_read_b128 v[0:3], v173 offset:1024
	ds_read_b128 v[4:7], v173 offset:2048
	ds_read_b128 v[8:11], v173 offset:3072
	ds_read_b128 v[12:15], v173 offset:4096
	ds_read_b128 v[16:19], v173 offset:5120
	ds_read_b128 v[20:23], v173 offset:6144
	ds_read_b128 v[24:27], v173 offset:7168
	s_waitcnt lgkmcnt(6)
	v_pk_add_f32 v[234:235], v[234:235], v[2:3]
	v_pk_add_f32 v[232:233], v[232:233], v[0:1]
	s_waitcnt lgkmcnt(5)
	v_pk_add_f32 v[234:235], v[234:235], v[6:7]
	v_pk_add_f32 v[232:233], v[232:233], v[4:5]
	s_waitcnt lgkmcnt(4)
	v_pk_add_f32 v[234:235], v[234:235], v[10:11]
	v_pk_add_f32 v[232:233], v[232:233], v[8:9]
	s_waitcnt lgkmcnt(3)
	v_pk_add_f32 v[234:235], v[234:235], v[14:15]
	v_pk_add_f32 v[232:233], v[232:233], v[12:13]
	s_waitcnt lgkmcnt(2)
	v_pk_add_f32 v[234:235], v[234:235], v[18:19]
	v_pk_add_f32 v[232:233], v[232:233], v[16:17]
	s_waitcnt lgkmcnt(1)
	v_pk_add_f32 v[234:235], v[234:235], v[22:23]
	v_pk_add_f32 v[232:233], v[232:233], v[20:21]
	s_waitcnt lgkmcnt(0)
	v_pk_add_f32 v[18:19], v[234:235], v[26:27]
	v_pk_add_f32 v[16:17], v[232:233], v[24:25]
	v_mul_f32_e32 v16, 0xbfb8aa3b, v16
	v_exp_f32_e32 v20, v16
	v_add_f32_e32 v16, v18, v18
	v_mul_f32_e32 v16, 0x3fb8aa3b, v16
	v_mul_f32_e32 v17, 0xbfb8aa3b, v17
	v_exp_f32_e32 v18, v16
	v_exp_f32_e32 v17, v17
	v_add_f32_e32 v18, 1.0, v18
	v_add_f32_e32 v16, 1.0, v17
	v_add_f32_e32 v17, 1.0, v20
	v_rcp_f32_e32 v18, v18
	v_rcp_f32_e32 v16, v16
	v_rcp_f32_e32 v173, v17
	v_fma_f32 v17, v18, -2.0, 1.0
	v_pk_mul_f32 v[16:17], v[172:173], v[16:17]
	s_nop 0
	v_add_f32_e32 v172, v16, v17
	v_add_f32_e32 v17, v172, v172
	v_mul_f32_e32 v17, 0x3fb8aa3b, v17
	v_mul_f32_e32 v16, 0xbfb8aa3b, v19
	v_exp_f32_e32 v17, v17
	v_exp_f32_e32 v16, v16
	v_add_f32_e32 v17, 1.0, v17
	v_add_f32_e32 v16, 1.0, v16
	v_rcp_f32_e32 v17, v17
	v_rcp_f32_e32 v16, v16
	v_fma_f32 v17, v17, -2.0, 1.0
	v_fma_mixlo_f16 v16, v16, v17, 0
	ds_write_b16 v171, v16
	s_and_saveexec_b64 s[10:11], s[4:5]
	s_cbranch_execz .Lrec_pubdone
	ds_read_b64 v[16:17], v195
	s_and_b32 s12, s36, 1
	s_lshl_b32 s12, s12, 18
	v_mov_b32_e32 v18, s12
	v_mov_b32_e32 v19, 0
	v_lshl_add_u64 v[20:21], v[240:241], 0, v[18:19]
	v_add_u32_e32 v18, s41, v185
	v_lshlrev_b64 v[18:19], 11, v[18:19]
	v_lshl_add_u64 v[22:23], v[180:181], 0, v[18:19]
	s_bfe_u32 s12, s36, 0x10001
	s_mul_i32 s12, s12, 0x40004000
	s_and_b64 vcc, exec, s[6:7]
	s_cbranch_vccz .Lrec_pubfast
	s_waitcnt lgkmcnt(0)
	v_or_b32_e32 v18, s12, v16
	v_or_b32_e32 v19, s12, v17
	global_store_dwordx2 v[20:21], v[18:19], off sc1
	global_store_dwordx2 v[22:23], v[16:17], off
	s_branch .Lrec_pubdone
.Lrec_pubfast:
	s_waitcnt lgkmcnt(0)
	v_or_b32_e32 v18, s12, v16
	v_or_b32_e32 v19, s12, v17
	global_store_dwordx2 v[20:21], v[18:19], off sc0
	global_store_dwordx2 v[22:23], v[16:17], off

	.amdhsa_kernel _Z15lstm_persistentPKDF16_PKfPDF16_PjS4_S2_S3_
		.amdhsa_group_segment_fixed_size 0
		.amdhsa_private_segment_fixed_size 0
		.amdhsa_kernarg_size 56
		.amdhsa_user_sgpr_count 2
		.amdhsa_user_sgpr_dispatch_ptr 0
		.amdhsa_user_sgpr_queue_ptr 0
		.amdhsa_user_sgpr_kernarg_segment_ptr 1
		.amdhsa_user_sgpr_dispatch_id 0
		.amdhsa_user_sgpr_kernarg_preload_length 0
		.amdhsa_user_sgpr_kernarg_preload_offset 0
		.amdhsa_user_sgpr_private_segment_size 0
		.amdhsa_uses_dynamic_stack 0
		.amdhsa_enable_private_segment 0
		.amdhsa_system_sgpr_workgroup_id_x 1
		.amdhsa_system_sgpr_workgroup_id_y 0
		.amdhsa_system_sgpr_workgroup_id_z 0
		.amdhsa_system_sgpr_workgroup_info 0
		.amdhsa_system_vgpr_workitem_id 0
		.amdhsa_next_free_vgpr 242
		.amdhsa_next_free_sgpr 49
		.amdhsa_accum_offset 244
		.amdhsa_reserve_vcc 1
		.amdhsa_float_round_mode_32 0
		.amdhsa_float_round_mode_16_64 0
		.amdhsa_float_denorm_mode_32 3
		.amdhsa_float_denorm_mode_16_64 3
		.amdhsa_dx10_clamp 1
		.amdhsa_ieee_mode 1
		.amdhsa_fp16_overflow 0
		.amdhsa_tg_split 0
		.amdhsa_exception_fp_ieee_invalid_op 0
		.amdhsa_exception_fp_denorm_src 0
		.amdhsa_exception_fp_ieee_div_zero 0
		.amdhsa_exception_fp_ieee_overflow 0
		.amdhsa_exception_fp_ieee_underflow 0
		.amdhsa_exception_fp_ieee_inexact 0
		.amdhsa_exception_int_div_zero 0
	.end_amdhsa_kernel

_Z11gemm_8phaseILi1EEvPKDF16_S1_PfPKfS4_:
	s_cmpk_gt_u32 s2, 0x2ef
	s_cbranch_scc1 .LBB5_23
	s_load_dwordx8 s[4:11], s[0:1], 0x0
	s_and_b32 s25, s2, 7
	s_lshr_b32 s24, s2, 3
	s_mulk_i32 s25, 0x5e
	s_add_i32 s3, s25, s24
	s_waitcnt lgkmcnt(0)
	s_mov_b32 s12, s4
	s_lshr_b32 s4, s3, 4
	v_lshlrev_b32_e32 v3, 4, v0
	v_and_b32_e32 v1, 32, v0
	s_and_b32 s21, s4, 0x78
	v_lshrrev_b32_e32 v4, 3, v0
	v_bfe_u32 v5, v0, 2, 4
	v_bitop3_b32 v1, v3, v1, 48 bitop3:0x6c
	v_and_b32_e32 v2, 64, v0
	s_sub_i32 s4, 47, s21
	v_and_or_b32 v6, v4, 48, v5
	v_or_b32_e32 v7, v2, v1
	s_min_i32 s4, s4, 8
	v_lshl_or_b32 v1, v6, 11, v7
	v_cvt_f32_i32_e32 v6, s4
	v_or_b32_e32 v4, 64, v4
	s_movk_i32 s2, 0x70
	v_and_or_b32 v4, v4, s2, v5
	v_lshl_or_b32 v114, v4, 11, v7
	v_rcp_iflag_f32_e32 v4, v6
	s_and_b32 s13, s5, 0xffff
	s_and_b32 s5, s3, 0x7f
	v_cvt_f32_ubyte0_e32 v5, s5
	v_mul_f32_e32 v4, v5, v4
	v_trunc_f32_e32 v4, v4
	s_ashr_i32 s2, s4, 30
	v_fma_f32 v5, -v4, v6, v5
	v_cvt_i32_f32_e32 v4, v4
	s_and_b32 s17, s7, 0xffff
	s_or_b32 s7, s2, 1
	v_cmp_ge_f32_e64 s[2:3], |v5|, |v6|
	s_and_b64 s[2:3], s[2:3], exec
	s_cselect_b32 s2, s7, 0
	s_add_i32 s7, 0, 0x10000
	v_readfirstlane_b32 s3, v4
	v_add_u32_e32 v115, s7, v3
	s_add_i32 s2, s3, s2
	v_readfirstlane_b32 s3, v115
	s_movk_i32 s22, 0x100
	s_sext_i32_i8 s20, s2
	s_mul_i32 s2, s2, s4
	s_mov_b32 m0, s3
	v_and_b32_e32 v5, 0xff0, v3
	s_add_i32 s3, 0, 0x1c000
	s_sub_i32 s2, s5, s2
	v_add_u32_e32 v4, 0x2000, v115
	v_add_u32_e32 v5, s3, v5
	v_cmp_gt_u32_e64 s[4:5], s22, v0
	s_mov_b32 s15, 0x20000
	s_and_b32 s2, s2, 0xff
	v_cndmask_b32_e64 v117, v5, v4, s[4:5]
	s_mov_b32 s18, 0x600000
	s_mov_b32 s16, s6
	s_mov_b32 s19, s15
	s_add_i32 s21, s21, s2
	s_mul_i32 s2, s20, 0x60000
	v_readfirstlane_b32 s3, v117
	v_add_u32_e32 v118, 0, v3
	buffer_load_dwordx4 v1, s[16:19], s2 offen lds
	v_cndmask_b32_e64 v116, v1, v114, s[4:5]
	s_mov_b32 m0, s3
	v_readfirstlane_b32 s22, v118
	v_add_u32_e32 v119, 0x2000, v118
	s_mov_b32 s14, 0x1780000
	buffer_load_dwordx4 v116, s[16:19], s2 offen lds
	s_lshl_b32 s3, s21, 19
	s_mov_b32 m0, s22
	v_readfirstlane_b32 s22, v119
	buffer_load_dwordx4 v1, s[12:15], s3 offen lds
	s_mov_b32 m0, s22
	s_add_i32 s22, 0, 0x13000
	v_add_u32_e32 v120, s22, v3
	v_add_u32_e32 v4, 0x2000, v120
	v_readfirstlane_b32 s26, v120
	v_cndmask_b32_e64 v121, v5, v4, s[4:5]
	buffer_load_dwordx4 v114, s[12:15], s3 offen lds
	s_add_i32 s23, s2, 0x30000
	s_mov_b32 m0, s26
	v_readfirstlane_b32 s26, v121
	v_add_u32_e32 v122, 0x4000, v118
	buffer_load_dwordx4 v1, s[16:19], s23 offen lds
	s_mov_b32 m0, s26
	v_readfirstlane_b32 s26, v122
	v_add_u32_e32 v123, 0x6000, v118
	buffer_load_dwordx4 v116, s[16:19], s23 offen lds
	s_or_b32 s23, s3, 0x40000
	s_mov_b32 m0, s26
	v_readfirstlane_b32 s26, v123
	buffer_load_dwordx4 v1, s[12:15], s23 offen lds
	s_mov_b32 m0, s26
	s_or_b32 s26, s2, 0x80
	buffer_load_dwordx4 v114, s[12:15], s23 offen lds
	s_add_i32 s23, 0, 0x16000
	v_add_u32_e32 v124, s23, v3
	v_add_u32_e32 v4, 0x2000, v124
	v_readfirstlane_b32 s27, v124
	v_cndmask_b32_e64 v125, v5, v4, s[4:5]
	s_mov_b32 m0, s27
	v_readfirstlane_b32 s27, v125
	buffer_load_dwordx4 v1, s[16:19], s26 offen lds
	s_mov_b32 m0, s27
	v_add_u32_e32 v126, 0x8000, v118
	buffer_load_dwordx4 v116, s[16:19], s26 offen lds
	v_readfirstlane_b32 s26, v126
	v_add_u32_e32 v127, 0xa000, v118
	s_add_i32 s28, 0, 0x19000
	s_bitset1_b32 s3, 7
	s_mov_b32 m0, s26
	v_readfirstlane_b32 s26, v127
	v_add_u32_e32 v128, s28, v3
	buffer_load_dwordx4 v1, s[12:15], s3 offen lds
	s_mov_b32 m0, s26
	v_add_u32_e32 v3, 0x2000, v128
	buffer_load_dwordx4 v114, s[12:15], s3 offen lds
	v_readfirstlane_b32 s3, v128
	v_cndmask_b32_e64 v129, v5, v3, s[4:5]
	s_add_i32 s2, s2, 0x30080
	s_mov_b32 m0, s3
	v_readfirstlane_b32 s3, v129
	buffer_load_dwordx4 v1, s[16:19], s2 offen lds
	s_mov_b32 m0, s3
	v_and_b32_e32 v4, 0x100, v0
	buffer_load_dwordx4 v116, s[16:19], s2 offen lds
	s_load_dword s16, s[0:1], 0x28
	v_lshrrev_b32_e32 v3, 2, v0
	s_movk_i32 s26, 0x80
	v_cmp_ne_u32_e64 s[2:3], 0, v4
	s_and_saveexec_b64 s[0:1], s[2:3]
	s_cbranch_execz .LBB5_3
	s_barrier

.LBB5_6:
	s_or_b32 s30, s29, 0x80
	s_lshl_b32 s0, s30, 11
	v_readfirstlane_b32 s6, v130
	s_or_b32 s1, s0, 0x80
	s_mov_b32 m0, s6
	v_readfirstlane_b32 s6, v131
	ds_read_b128 v[2:5], v132
	ds_read_b128 v[6:9], v132 offset:1024
	ds_read_b128 v[10:13], v133
	ds_read_b128 v[14:17], v133 offset:1024
	ds_read_b128 v[18:21], v134
	ds_read_b128 v[22:25], v134 offset:1024
	buffer_load_dwordx4 v1, s[12:15], s1 offen lds
	s_mov_b32 m0, s6
	s_mov_b32 s31, s33
	buffer_load_dwordx4 v114, s[12:15], s1 offen lds
	ds_read_b128 v[26:29], v135
	ds_read_b128 v[30:33], v135 offset:1024
	ds_read_b128 v[34:37], v136
	ds_read_b128 v[38:41], v136 offset:1024
	ds_read_b128 v[42:45], v137
	ds_read_b128 v[46:49], v137 offset:1024
	ds_read_b128 v[50:53], v138
	ds_read_b128 v[54:57], v138 offset:1024
	ds_read_b128 v[58:61], v138 offset:2048
	ds_read_b128 v[62:65], v139 offset:3072
	s_waitcnt lgkmcnt(0)
	s_barrier
	s_setprio 1
	s_waitcnt lgkmcnt(3)
	v_mfma_f32_16x16x32_f16 v[66:69], v[50:53], v[2:5], 0
	v_mfma_f32_16x16x32_f16 v[70:73], v[50:53], v[10:13], 0
	v_mfma_f32_16x16x32_f16 v[74:77], v[50:53], v[18:21], 0
	s_waitcnt lgkmcnt(1)
	v_mfma_f32_16x16x32_f16 v[78:81], v[58:61], v[2:5], 0
	v_mfma_f32_16x16x32_f16 v[82:85], v[58:61], v[10:13], 0
	v_mfma_f32_16x16x32_f16 v[86:89], v[58:61], v[18:21], 0
	v_mfma_f32_16x16x32_f16 v[66:69], v[54:57], v[6:9], v[66:69]
	v_mfma_f32_16x16x32_f16 v[70:73], v[54:57], v[14:17], v[70:73]
	v_mfma_f32_16x16x32_f16 v[74:77], v[54:57], v[22:25], v[74:77]
	s_waitcnt lgkmcnt(0)
	v_mfma_f32_16x16x32_f16 v[78:81], v[62:65], v[6:9], v[78:81]
	v_mfma_f32_16x16x32_f16 v[82:85], v[62:65], v[14:17], v[82:85]
	v_mfma_f32_16x16x32_f16 v[86:89], v[62:65], v[22:25], v[86:89]
	s_setprio 0
	s_setprio 1
	v_mfma_f32_16x16x32_f16 v[90:93], v[50:53], v[26:29], 0
	v_mfma_f32_16x16x32_f16 v[94:97], v[50:53], v[34:37], 0
	v_mfma_f32_16x16x32_f16 v[50:53], v[50:53], v[42:45], 0
	v_mfma_f32_16x16x32_f16 v[90:93], v[54:57], v[30:33], v[90:93]
	v_mfma_f32_16x16x32_f16 v[94:97], v[54:57], v[38:41], v[94:97]
	v_mfma_f32_16x16x32_f16 v[50:53], v[54:57], v[46:49], v[50:53]
	v_mfma_f32_16x16x32_f16 v[54:57], v[58:61], v[26:29], 0
	v_mfma_f32_16x16x32_f16 v[98:101], v[58:61], v[34:37], 0
	v_mfma_f32_16x16x32_f16 v[58:61], v[58:61], v[42:45], 0
	v_mfma_f32_16x16x32_f16 v[54:57], v[62:65], v[30:33], v[54:57]
	v_mfma_f32_16x16x32_f16 v[58:61], v[62:65], v[46:49], v[58:61]
	v_mfma_f32_16x16x32_f16 v[98:101], v[62:65], v[38:41], v[98:101]
	s_setprio 0
	s_barrier
	s_lshl_b32 s1, s33, 11
	v_readfirstlane_b32 s7, v115
	s_or_b32 s6, s1, 0x100
	s_mov_b32 m0, s7
	v_readfirstlane_b32 s7, v117
	ds_read_b128 v[62:65], v138 offset:16384
	ds_read_b128 v[102:105], v138 offset:17408
	ds_read_b128 v[106:109], v138 offset:18432
	ds_read_b128 v[110:113], v139 offset:19456
	buffer_load_dwordx4 v1, s[16:19], s6 offen lds
	s_mov_b32 m0, s7
	v_readfirstlane_b32 s7, v120
	buffer_load_dwordx4 v116, s[16:19], s6 offen lds
	s_add_i32 s6, s1, 0x30100
	s_mov_b32 m0, s7
	v_readfirstlane_b32 s7, v121
	buffer_load_dwordx4 v1, s[16:19], s6 offen lds
	s_mov_b32 m0, s7
	v_readfirstlane_b32 s33, v118
	buffer_load_dwordx4 v116, s[16:19], s6 offen lds
	s_lshl_b32 s6, s29, 11
	s_or_b32 s7, s6, 0x100
	s_mov_b32 m0, s33
	v_readfirstlane_b32 s33, v119
	buffer_load_dwordx4 v1, s[12:15], s7 offen lds
	s_mov_b32 m0, s33
	s_nop 0
	buffer_load_dwordx4 v114, s[12:15], s7 offen lds
	s_waitcnt lgkmcnt(0)
	s_barrier
	s_setprio 1
	s_waitcnt lgkmcnt(3)
	v_mfma_f32_16x16x32_f16 v[146:149], v[62:65], v[2:5], 0
	s_waitcnt lgkmcnt(1)
	v_mfma_f32_16x16x32_f16 v[2:5], v[106:109], v[2:5], 0
	s_waitcnt lgkmcnt(0)
	v_mfma_f32_16x16x32_f16 v[158:161], v[110:113], v[6:9], v[2:5]
	v_mfma_f32_16x16x32_f16 v[2:5], v[106:109], v[10:13], 0
	v_mfma_f32_16x16x32_f16 v[150:153], v[62:65], v[10:13], 0
	v_mfma_f32_16x16x32_f16 v[154:157], v[62:65], v[18:21], 0
	v_mfma_f32_16x16x32_f16 v[162:165], v[110:113], v[14:17], v[2:5]
	v_mfma_f32_16x16x32_f16 v[2:5], v[106:109], v[18:21], 0
	v_mfma_f32_16x16x32_f16 v[146:149], v[102:105], v[6:9], v[146:149]
	v_mfma_f32_16x16x32_f16 v[150:153], v[102:105], v[14:17], v[150:153]
	v_mfma_f32_16x16x32_f16 v[154:157], v[102:105], v[22:25], v[154:157]
	v_mfma_f32_16x16x32_f16 v[166:169], v[110:113], v[22:25], v[2:5]
	s_setprio 0
	s_setprio 1
	v_mfma_f32_16x16x32_f16 v[2:5], v[62:65], v[26:29], 0
	v_mfma_f32_16x16x32_f16 v[170:173], v[102:105], v[30:33], v[2:5]
	v_mfma_f32_16x16x32_f16 v[2:5], v[62:65], v[34:37], 0
	v_mfma_f32_16x16x32_f16 v[174:177], v[102:105], v[38:41], v[2:5]
	v_mfma_f32_16x16x32_f16 v[2:5], v[62:65], v[42:45], 0
	v_mfma_f32_16x16x32_f16 v[62:65], v[102:105], v[46:49], v[2:5]
	v_mfma_f32_16x16x32_f16 v[2:5], v[106:109], v[26:29], 0
	v_mfma_f32_16x16x32_f16 v[102:105], v[110:113], v[30:33], v[2:5]
	v_mfma_f32_16x16x32_f16 v[2:5], v[106:109], v[34:37], 0
	v_mfma_f32_16x16x32_f16 v[178:181], v[110:113], v[38:41], v[2:5]
	v_mfma_f32_16x16x32_f16 v[2:5], v[106:109], v[42:45], 0
	v_mfma_f32_16x16x32_f16 v[106:109], v[110:113], v[46:49], v[2:5]
	s_setprio 0
	s_barrier
	v_readfirstlane_b32 s33, v122
	s_or_b32 s7, s0, 0x100
	s_mov_b32 m0, s33
	v_readfirstlane_b32 s33, v123
	s_nop 0
	ds_read_b128 v[2:5], v138 offset:32768
	ds_read_b128 v[6:9], v138 offset:33792
	ds_read_b128 v[110:113], v138 offset:34816
	ds_read_b128 v[182:185], v139 offset:35840
	buffer_load_dwordx4 v1, s[12:15], s7 offen lds
	s_mov_b32 m0, s33
	s_nop 0
	buffer_load_dwordx4 v114, s[12:15], s7 offen lds
	ds_read_b128 v[186:189], v140
	ds_read_b128 v[190:193], v140 offset:1024
	ds_read_b128 v[194:197], v141
	ds_read_b128 v[198:201], v141 offset:1024
	ds_read_b128 v[202:205], v142
	ds_read_b128 v[206:209], v142 offset:1024
	ds_read_b128 v[210:213], v143
	ds_read_b128 v[214:217], v143 offset:1024
	ds_read_b128 v[218:221], v144
	ds_read_b128 v[222:225], v144 offset:1024
	ds_read_b128 v[226:229], v145
	ds_read_b128 v[230:233], v145 offset:1024
	s_waitcnt vmcnt(8)
	s_waitcnt lgkmcnt(0)
	s_barrier
	s_setprio 1
	s_waitcnt lgkmcnt(11)
	v_mfma_f32_16x16x32_f16 v[10:13], v[2:5], v[186:189], v[66:69]
	s_waitcnt lgkmcnt(10)
	v_mfma_f32_16x16x32_f16 v[46:49], v[6:9], v[190:193], v[10:13]
	s_waitcnt lgkmcnt(9)
	v_mfma_f32_16x16x32_f16 v[10:13], v[2:5], v[194:197], v[70:73]
	s_waitcnt lgkmcnt(8)
	v_mfma_f32_16x16x32_f16 v[42:45], v[6:9], v[198:201], v[10:13]
	s_waitcnt lgkmcnt(7)
	v_mfma_f32_16x16x32_f16 v[10:13], v[2:5], v[202:205], v[74:77]
	s_waitcnt lgkmcnt(6)
	v_mfma_f32_16x16x32_f16 v[38:41], v[6:9], v[206:209], v[10:13]
	v_mfma_f32_16x16x32_f16 v[10:13], v[110:113], v[186:189], v[78:81]
	v_mfma_f32_16x16x32_f16 v[34:37], v[182:185], v[190:193], v[10:13]
	v_mfma_f32_16x16x32_f16 v[10:13], v[110:113], v[194:197], v[82:85]
	v_mfma_f32_16x16x32_f16 v[30:33], v[182:185], v[198:201], v[10:13]
	v_mfma_f32_16x16x32_f16 v[10:13], v[110:113], v[202:205], v[86:89]
	v_mfma_f32_16x16x32_f16 v[26:29], v[182:185], v[206:209], v[10:13]
	s_setprio 0
	s_setprio 1
	s_waitcnt lgkmcnt(5)
	v_mfma_f32_16x16x32_f16 v[10:13], v[2:5], v[210:213], v[90:93]
	s_waitcnt lgkmcnt(4)
	v_mfma_f32_16x16x32_f16 v[22:25], v[6:9], v[214:217], v[10:13]
	s_waitcnt lgkmcnt(3)
	v_mfma_f32_16x16x32_f16 v[10:13], v[2:5], v[218:221], v[94:97]
	s_waitcnt lgkmcnt(1)
	v_mfma_f32_16x16x32_f16 v[2:5], v[2:5], v[226:229], v[50:53]
	s_waitcnt lgkmcnt(0)
	v_mfma_f32_16x16x32_f16 v[14:17], v[6:9], v[230:233], v[2:5]
	v_mfma_f32_16x16x32_f16 v[2:5], v[110:113], v[210:213], v[54:57]
	v_mfma_f32_16x16x32_f16 v[18:21], v[6:9], v[222:225], v[10:13]
	v_mfma_f32_16x16x32_f16 v[10:13], v[182:185], v[214:217], v[2:5]
	v_mfma_f32_16x16x32_f16 v[2:5], v[110:113], v[218:221], v[98:101]
	v_mfma_f32_16x16x32_f16 v[6:9], v[182:185], v[222:225], v[2:5]
	v_mfma_f32_16x16x32_f16 v[2:5], v[110:113], v[226:229], v[58:61]
	v_mfma_f32_16x16x32_f16 v[2:5], v[182:185], v[230:233], v[2:5]
	s_setprio 0
	s_barrier
	v_readfirstlane_b32 s33, v124
	s_or_b32 s7, s1, 0x180
	s_mov_b32 m0, s33
	v_readfirstlane_b32 s33, v125
	ds_read_b128 v[50:53], v138 offset:49152
	ds_read_b128 v[54:57], v138 offset:50176
	ds_read_b128 v[98:101], v138 offset:51200
	ds_read_b128 v[110:113], v139 offset:52224
	buffer_load_dwordx4 v1, s[16:19], s7 offen lds
	s_mov_b32 m0, s33
	v_readfirstlane_b32 s33, v128
	buffer_load_dwordx4 v116, s[16:19], s7 offen lds
	s_add_i32 s7, s1, 0x30180
	s_mov_b32 m0, s33
	v_readfirstlane_b32 s33, v129
	buffer_load_dwordx4 v1, s[16:19], s7 offen lds
	s_mov_b32 m0, s33
	v_readfirstlane_b32 s33, v126
	buffer_load_dwordx4 v116, s[16:19], s7 offen lds
	s_or_b32 s7, s6, 0x180
	s_mov_b32 m0, s33
	v_readfirstlane_b32 s33, v127
	buffer_load_dwordx4 v1, s[12:15], s7 offen lds
	s_mov_b32 m0, s33
	s_nop 0
	buffer_load_dwordx4 v114, s[12:15], s7 offen lds
	s_waitcnt vmcnt(8)
	s_waitcnt lgkmcnt(0)
	s_barrier
	s_setprio 1
	s_waitcnt lgkmcnt(3)
	v_mfma_f32_16x16x32_f16 v[58:61], v[50:53], v[186:189], v[146:149]
	s_waitcnt lgkmcnt(2)
	v_mfma_f32_16x16x32_f16 v[94:97], v[54:57], v[190:193], v[58:61]
	v_mfma_f32_16x16x32_f16 v[58:61], v[50:53], v[194:197], v[150:153]
	v_mfma_f32_16x16x32_f16 v[90:93], v[54:57], v[198:201], v[58:61]
	v_mfma_f32_16x16x32_f16 v[58:61], v[50:53], v[202:205], v[154:157]
	v_mfma_f32_16x16x32_f16 v[86:89], v[54:57], v[206:209], v[58:61]
	s_waitcnt lgkmcnt(1)
	v_mfma_f32_16x16x32_f16 v[58:61], v[98:101], v[186:189], v[158:161]
	s_waitcnt lgkmcnt(0)
	v_mfma_f32_16x16x32_f16 v[82:85], v[110:113], v[190:193], v[58:61]
	v_mfma_f32_16x16x32_f16 v[58:61], v[98:101], v[194:197], v[162:165]
	v_mfma_f32_16x16x32_f16 v[78:81], v[110:113], v[198:201], v[58:61]
	v_mfma_f32_16x16x32_f16 v[58:61], v[98:101], v[202:205], v[166:169]
	v_mfma_f32_16x16x32_f16 v[74:77], v[110:113], v[206:209], v[58:61]
	s_setprio 0
	s_setprio 1
	v_mfma_f32_16x16x32_f16 v[58:61], v[50:53], v[210:213], v[170:173]
	v_mfma_f32_16x16x32_f16 v[70:73], v[54:57], v[214:217], v[58:61]
	v_mfma_f32_16x16x32_f16 v[58:61], v[50:53], v[218:221], v[174:177]
	v_mfma_f32_16x16x32_f16 v[50:53], v[50:53], v[226:229], v[62:65]
	v_mfma_f32_16x16x32_f16 v[62:65], v[54:57], v[230:233], v[50:53]
	v_mfma_f32_16x16x32_f16 v[50:53], v[98:101], v[210:213], v[102:105]
	v_mfma_f32_16x16x32_f16 v[66:69], v[54:57], v[222:225], v[58:61]
	v_mfma_f32_16x16x32_f16 v[58:61], v[110:113], v[214:217], v[50:53]
	v_mfma_f32_16x16x32_f16 v[50:53], v[98:101], v[218:221], v[178:181]
	v_mfma_f32_16x16x32_f16 v[54:57], v[110:113], v[222:225], v[50:53]
	v_mfma_f32_16x16x32_f16 v[50:53], v[98:101], v[226:229], v[106:109]
	v_mfma_f32_16x16x32_f16 v[50:53], v[110:113], v[230:233], v[50:53]
	s_setprio 0
	s_barrier
	s_mov_b32 s7, 0
	s_mov_b32 s33, 0
.LBB5_7:
	s_add_i32 s34, s6, s7
	v_readfirstlane_b32 s36, v130
	s_add_i32 s35, s34, 0x40180
	s_mov_b32 m0, s36
	v_readfirstlane_b32 s36, v131
	ds_read_b128 v[98:101], v132
	ds_read_b128 v[102:105], v132 offset:1024
	ds_read_b128 v[106:109], v133
	ds_read_b128 v[110:113], v133 offset:1024
	ds_read_b128 v[146:149], v134
	ds_read_b128 v[150:153], v134 offset:1024
	buffer_load_dwordx4 v1, s[12:15], s35 offen lds
	s_mov_b32 m0, s36
	s_nop 0
	buffer_load_dwordx4 v114, s[12:15], s35 offen lds
	ds_read_b128 v[154:157], v135
	ds_read_b128 v[158:161], v135 offset:1024
	ds_read_b128 v[162:165], v136
	ds_read_b128 v[166:169], v136 offset:1024
	ds_read_b128 v[170:173], v137
	ds_read_b128 v[174:177], v137 offset:1024
	ds_read_b128 v[178:181], v138
	ds_read_b128 v[182:185], v138 offset:1024
	ds_read_b128 v[186:189], v138 offset:2048
	ds_read_b128 v[190:193], v139 offset:3072
	s_waitcnt vmcnt(8)
	s_waitcnt lgkmcnt(0)
	s_barrier
	s_setprio 1
	s_waitcnt lgkmcnt(3)
	v_mfma_f32_16x16x32_f16 v[46:49], v[178:181], v[98:101], v[46:49]
	v_mfma_f32_16x16x32_f16 v[42:45], v[178:181], v[106:109], v[42:45]
	v_mfma_f32_16x16x32_f16 v[38:41], v[178:181], v[146:149], v[38:41]
	s_waitcnt lgkmcnt(1)
	v_mfma_f32_16x16x32_f16 v[34:37], v[186:189], v[98:101], v[34:37]
	v_mfma_f32_16x16x32_f16 v[30:33], v[186:189], v[106:109], v[30:33]
	v_mfma_f32_16x16x32_f16 v[26:29], v[186:189], v[146:149], v[26:29]
	v_mfma_f32_16x16x32_f16 v[46:49], v[182:185], v[102:105], v[46:49]
	v_mfma_f32_16x16x32_f16 v[42:45], v[182:185], v[110:113], v[42:45]
	v_mfma_f32_16x16x32_f16 v[38:41], v[182:185], v[150:153], v[38:41]
	s_waitcnt lgkmcnt(0)
	v_mfma_f32_16x16x32_f16 v[34:37], v[190:193], v[102:105], v[34:37]
	v_mfma_f32_16x16x32_f16 v[30:33], v[190:193], v[110:113], v[30:33]
	v_mfma_f32_16x16x32_f16 v[26:29], v[190:193], v[150:153], v[26:29]
	s_setprio 0
	s_setprio 1
	v_mfma_f32_16x16x32_f16 v[22:25], v[178:181], v[154:157], v[22:25]
	v_mfma_f32_16x16x32_f16 v[18:21], v[178:181], v[162:165], v[18:21]
	v_mfma_f32_16x16x32_f16 v[14:17], v[178:181], v[170:173], v[14:17]
	v_mfma_f32_16x16x32_f16 v[10:13], v[186:189], v[154:157], v[10:13]
	v_mfma_f32_16x16x32_f16 v[6:9], v[186:189], v[162:165], v[6:9]
	v_mfma_f32_16x16x32_f16 v[2:5], v[186:189], v[170:173], v[2:5]
	v_mfma_f32_16x16x32_f16 v[22:25], v[182:185], v[158:161], v[22:25]
	v_mfma_f32_16x16x32_f16 v[18:21], v[182:185], v[166:169], v[18:21]
	v_mfma_f32_16x16x32_f16 v[14:17], v[182:185], v[174:177], v[14:17]
	v_mfma_f32_16x16x32_f16 v[10:13], v[190:193], v[158:161], v[10:13]
	v_mfma_f32_16x16x32_f16 v[6:9], v[190:193], v[166:169], v[6:9]
	v_mfma_f32_16x16x32_f16 v[2:5], v[190:193], v[174:177], v[2:5]
	s_setprio 0
	s_barrier
	s_add_i32 s35, s1, s7
	v_readfirstlane_b32 s37, v115
	s_add_i32 s36, s35, 0x200
	s_mov_b32 m0, s37
	v_readfirstlane_b32 s37, v117
	ds_read_b128 v[178:181], v138 offset:16384
	ds_read_b128 v[182:185], v138 offset:17408
	ds_read_b128 v[186:189], v138 offset:18432
	ds_read_b128 v[190:193], v139 offset:19456
	buffer_load_dwordx4 v1, s[16:19], s36 offen lds
	s_mov_b32 m0, s37
	v_readfirstlane_b32 s37, v120
	buffer_load_dwordx4 v116, s[16:19], s36 offen lds
	s_add_i32 s36, s35, 0x30200
	s_mov_b32 m0, s37
	v_readfirstlane_b32 s37, v121
	buffer_load_dwordx4 v1, s[16:19], s36 offen lds
	s_mov_b32 m0, s37
	v_readfirstlane_b32 s37, v118
	buffer_load_dwordx4 v116, s[16:19], s36 offen lds
	s_add_i32 s36, s34, 0x200
	s_mov_b32 m0, s37
	v_readfirstlane_b32 s37, v119
	buffer_load_dwordx4 v1, s[12:15], s36 offen lds
	s_mov_b32 m0, s37
	s_nop 0
	buffer_load_dwordx4 v114, s[12:15], s36 offen lds
	s_waitcnt vmcnt(8)
	s_waitcnt lgkmcnt(0)
	s_barrier
	s_setprio 1
	s_waitcnt lgkmcnt(3)
	v_mfma_f32_16x16x32_f16 v[94:97], v[178:181], v[98:101], v[94:97]
	v_mfma_f32_16x16x32_f16 v[90:93], v[178:181], v[106:109], v[90:93]
	v_mfma_f32_16x16x32_f16 v[86:89], v[178:181], v[146:149], v[86:89]
	s_waitcnt lgkmcnt(1)
	v_mfma_f32_16x16x32_f16 v[82:85], v[186:189], v[98:101], v[82:85]
	v_mfma_f32_16x16x32_f16 v[78:81], v[186:189], v[106:109], v[78:81]
	v_mfma_f32_16x16x32_f16 v[74:77], v[186:189], v[146:149], v[74:77]
	v_mfma_f32_16x16x32_f16 v[94:97], v[182:185], v[102:105], v[94:97]
	v_mfma_f32_16x16x32_f16 v[90:93], v[182:185], v[110:113], v[90:93]
	v_mfma_f32_16x16x32_f16 v[86:89], v[182:185], v[150:153], v[86:89]
	s_waitcnt lgkmcnt(0)
	v_mfma_f32_16x16x32_f16 v[82:85], v[190:193], v[102:105], v[82:85]
	v_mfma_f32_16x16x32_f16 v[78:81], v[190:193], v[110:113], v[78:81]
	v_mfma_f32_16x16x32_f16 v[74:77], v[190:193], v[150:153], v[74:77]
	s_setprio 0
	s_setprio 1
	v_mfma_f32_16x16x32_f16 v[70:73], v[178:181], v[154:157], v[70:73]
	v_mfma_f32_16x16x32_f16 v[66:69], v[178:181], v[162:165], v[66:69]
	v_mfma_f32_16x16x32_f16 v[62:65], v[178:181], v[170:173], v[62:65]
	v_mfma_f32_16x16x32_f16 v[58:61], v[186:189], v[154:157], v[58:61]
	v_mfma_f32_16x16x32_f16 v[54:57], v[186:189], v[162:165], v[54:57]
	v_mfma_f32_16x16x32_f16 v[50:53], v[186:189], v[170:173], v[50:53]
	v_mfma_f32_16x16x32_f16 v[70:73], v[182:185], v[158:161], v[70:73]
	v_mfma_f32_16x16x32_f16 v[66:69], v[182:185], v[166:169], v[66:69]
	v_mfma_f32_16x16x32_f16 v[62:65], v[182:185], v[174:177], v[62:65]
	v_mfma_f32_16x16x32_f16 v[58:61], v[190:193], v[158:161], v[58:61]
	v_mfma_f32_16x16x32_f16 v[54:57], v[190:193], v[166:169], v[54:57]
	v_mfma_f32_16x16x32_f16 v[50:53], v[190:193], v[174:177], v[50:53]
	s_setprio 0
	s_barrier
	v_readfirstlane_b32 s37, v122
	s_add_i32 s36, s34, 0x40200
	s_mov_b32 m0, s37
	v_readfirstlane_b32 s37, v123
	ds_read_b128 v[98:101], v138 offset:32768
	ds_read_b128 v[102:105], v138 offset:33792
	ds_read_b128 v[106:109], v138 offset:34816
	ds_read_b128 v[110:113], v139 offset:35840
	buffer_load_dwordx4 v1, s[12:15], s36 offen lds
	s_mov_b32 m0, s37
	s_nop 0
	buffer_load_dwordx4 v114, s[12:15], s36 offen lds
	ds_read_b128 v[146:149], v140
	ds_read_b128 v[150:153], v140 offset:1024
	ds_read_b128 v[154:157], v141
	ds_read_b128 v[158:161], v141 offset:1024
	ds_read_b128 v[162:165], v142
	ds_read_b128 v[166:169], v142 offset:1024
	ds_read_b128 v[170:173], v143
	ds_read_b128 v[174:177], v143 offset:1024
	ds_read_b128 v[178:181], v144
	ds_read_b128 v[182:185], v144 offset:1024
	ds_read_b128 v[186:189], v145
	ds_read_b128 v[190:193], v145 offset:1024
	s_waitcnt vmcnt(8)
	s_waitcnt lgkmcnt(0)
	s_barrier
	s_setprio 1
	s_waitcnt lgkmcnt(11)
	v_mfma_f32_16x16x32_f16 v[46:49], v[98:101], v[146:149], v[46:49]
	s_waitcnt lgkmcnt(9)
	v_mfma_f32_16x16x32_f16 v[42:45], v[98:101], v[154:157], v[42:45]
	s_waitcnt lgkmcnt(7)
	v_mfma_f32_16x16x32_f16 v[38:41], v[98:101], v[162:165], v[38:41]
	v_mfma_f32_16x16x32_f16 v[34:37], v[106:109], v[146:149], v[34:37]
	v_mfma_f32_16x16x32_f16 v[30:33], v[106:109], v[154:157], v[30:33]
	v_mfma_f32_16x16x32_f16 v[26:29], v[106:109], v[162:165], v[26:29]
	v_mfma_f32_16x16x32_f16 v[46:49], v[102:105], v[150:153], v[46:49]
	v_mfma_f32_16x16x32_f16 v[42:45], v[102:105], v[158:161], v[42:45]
	s_waitcnt lgkmcnt(6)
	v_mfma_f32_16x16x32_f16 v[38:41], v[102:105], v[166:169], v[38:41]
	v_mfma_f32_16x16x32_f16 v[34:37], v[110:113], v[150:153], v[34:37]
	v_mfma_f32_16x16x32_f16 v[30:33], v[110:113], v[158:161], v[30:33]
	v_mfma_f32_16x16x32_f16 v[26:29], v[110:113], v[166:169], v[26:29]
	s_setprio 0
	s_setprio 1
	s_waitcnt lgkmcnt(5)
	v_mfma_f32_16x16x32_f16 v[22:25], v[98:101], v[170:173], v[22:25]
	s_waitcnt lgkmcnt(3)
	v_mfma_f32_16x16x32_f16 v[18:21], v[98:101], v[178:181], v[18:21]
	s_waitcnt lgkmcnt(1)
	v_mfma_f32_16x16x32_f16 v[14:17], v[98:101], v[186:189], v[14:17]
	v_mfma_f32_16x16x32_f16 v[10:13], v[106:109], v[170:173], v[10:13]
	v_mfma_f32_16x16x32_f16 v[6:9], v[106:109], v[178:181], v[6:9]
	v_mfma_f32_16x16x32_f16 v[2:5], v[106:109], v[186:189], v[2:5]
	v_mfma_f32_16x16x32_f16 v[22:25], v[102:105], v[174:177], v[22:25]
	v_mfma_f32_16x16x32_f16 v[18:21], v[102:105], v[182:185], v[18:21]
	s_waitcnt lgkmcnt(0)
	v_mfma_f32_16x16x32_f16 v[14:17], v[102:105], v[190:193], v[14:17]
	v_mfma_f32_16x16x32_f16 v[10:13], v[110:113], v[174:177], v[10:13]
	v_mfma_f32_16x16x32_f16 v[6:9], v[110:113], v[182:185], v[6:9]
	v_mfma_f32_16x16x32_f16 v[2:5], v[110:113], v[190:193], v[2:5]
	s_setprio 0
	s_barrier
	v_readfirstlane_b32 s37, v124
	s_add_i32 s36, s35, 0x280
	s_mov_b32 m0, s37
	v_readfirstlane_b32 s37, v125
	ds_read_b128 v[98:101], v138 offset:49152
	ds_read_b128 v[102:105], v138 offset:50176
	ds_read_b128 v[106:109], v138 offset:51200
	ds_read_b128 v[110:113], v139 offset:52224
	buffer_load_dwordx4 v1, s[16:19], s36 offen lds
	s_mov_b32 m0, s37
	s_add_i32 s35, s35, 0x30280
	buffer_load_dwordx4 v116, s[16:19], s36 offen lds
	v_readfirstlane_b32 s36, v128
	s_mov_b32 m0, s36
	v_readfirstlane_b32 s36, v129
	buffer_load_dwordx4 v1, s[16:19], s35 offen lds
	s_mov_b32 m0, s36
	s_addk_i32 s34, 0x280
	buffer_load_dwordx4 v116, s[16:19], s35 offen lds
	v_readfirstlane_b32 s35, v126
	s_mov_b32 m0, s35
	v_readfirstlane_b32 s35, v127
	buffer_load_dwordx4 v1, s[12:15], s34 offen lds
	s_mov_b32 m0, s35
	s_nop 0
	buffer_load_dwordx4 v114, s[12:15], s34 offen lds
	s_waitcnt vmcnt(8)
	s_waitcnt lgkmcnt(0)
	s_barrier
	s_setprio 1
	s_waitcnt lgkmcnt(3)
	v_mfma_f32_16x16x32_f16 v[94:97], v[98:101], v[146:149], v[94:97]
	v_mfma_f32_16x16x32_f16 v[90:93], v[98:101], v[154:157], v[90:93]
	v_mfma_f32_16x16x32_f16 v[86:89], v[98:101], v[162:165], v[86:89]
	s_waitcnt lgkmcnt(1)
	v_mfma_f32_16x16x32_f16 v[82:85], v[106:109], v[146:149], v[82:85]
	v_mfma_f32_16x16x32_f16 v[78:81], v[106:109], v[154:157], v[78:81]
	v_mfma_f32_16x16x32_f16 v[74:77], v[106:109], v[162:165], v[74:77]
	v_mfma_f32_16x16x32_f16 v[94:97], v[102:105], v[150:153], v[94:97]
	v_mfma_f32_16x16x32_f16 v[90:93], v[102:105], v[158:161], v[90:93]
	v_mfma_f32_16x16x32_f16 v[86:89], v[102:105], v[166:169], v[86:89]
	s_waitcnt lgkmcnt(0)
	v_mfma_f32_16x16x32_f16 v[82:85], v[110:113], v[150:153], v[82:85]
	v_mfma_f32_16x16x32_f16 v[78:81], v[110:113], v[158:161], v[78:81]
	v_mfma_f32_16x16x32_f16 v[74:77], v[110:113], v[166:169], v[74:77]
	s_setprio 0
	s_setprio 1
	v_mfma_f32_16x16x32_f16 v[70:73], v[98:101], v[170:173], v[70:73]
	v_mfma_f32_16x16x32_f16 v[66:69], v[98:101], v[178:181], v[66:69]
	v_mfma_f32_16x16x32_f16 v[62:65], v[98:101], v[186:189], v[62:65]
	v_mfma_f32_16x16x32_f16 v[58:61], v[106:109], v[170:173], v[58:61]
	v_mfma_f32_16x16x32_f16 v[54:57], v[106:109], v[178:181], v[54:57]
	v_mfma_f32_16x16x32_f16 v[50:53], v[106:109], v[186:189], v[50:53]
	v_mfma_f32_16x16x32_f16 v[70:73], v[102:105], v[174:177], v[70:73]
	v_mfma_f32_16x16x32_f16 v[66:69], v[102:105], v[182:185], v[66:69]
	v_mfma_f32_16x16x32_f16 v[62:65], v[102:105], v[190:193], v[62:65]
	v_mfma_f32_16x16x32_f16 v[58:61], v[110:113], v[174:177], v[58:61]
	v_mfma_f32_16x16x32_f16 v[54:57], v[110:113], v[182:185], v[54:57]
	v_mfma_f32_16x16x32_f16 v[50:53], v[110:113], v[190:193], v[50:53]
	s_setprio 0
	s_barrier
	s_add_i32 s33, s33, 2
	s_addk_i32 s7, 0x100
	s_cmp_lt_u32 s33, 12
	s_cbranch_scc1 .LBB5_7
	v_readfirstlane_b32 s1, v130
	s_or_b32 s0, s0, 0x780
	s_mov_b32 m0, s1
	v_readfirstlane_b32 s1, v131
	ds_read_b128 v[98:101], v132
	ds_read_b128 v[102:105], v132 offset:1024
	ds_read_b128 v[106:109], v133
	ds_read_b128 v[110:113], v133 offset:1024
	ds_read_b128 v[146:149], v134
	ds_read_b128 v[150:153], v134 offset:1024
	buffer_load_dwordx4 v1, s[12:15], s0 offen lds
	s_mov_b32 m0, s1
	s_nop 0
	buffer_load_dwordx4 v114, s[12:15], s0 offen lds
	ds_read_b128 v[154:157], v135
	ds_read_b128 v[158:161], v135 offset:1024
	ds_read_b128 v[162:165], v136
	ds_read_b128 v[166:169], v136 offset:1024
	ds_read_b128 v[170:173], v137
	ds_read_b128 v[174:177], v137 offset:1024
	ds_read_b128 v[178:181], v138
	ds_read_b128 v[182:185], v138 offset:1024
	ds_read_b128 v[186:189], v138 offset:2048
	ds_read_b128 v[190:193], v139 offset:3072
	s_waitcnt vmcnt(8)
	s_waitcnt lgkmcnt(0)
	s_barrier
	s_setprio 1
	s_waitcnt lgkmcnt(3)
	v_mfma_f32_16x16x32_f16 v[46:49], v[178:181], v[98:101], v[46:49]
	v_mfma_f32_16x16x32_f16 v[42:45], v[178:181], v[106:109], v[42:45]
	v_mfma_f32_16x16x32_f16 v[38:41], v[178:181], v[146:149], v[38:41]
	s_waitcnt lgkmcnt(1)
	v_mfma_f32_16x16x32_f16 v[34:37], v[186:189], v[98:101], v[34:37]
	v_mfma_f32_16x16x32_f16 v[30:33], v[186:189], v[106:109], v[30:33]
	v_mfma_f32_16x16x32_f16 v[26:29], v[186:189], v[146:149], v[26:29]
	v_mfma_f32_16x16x32_f16 v[46:49], v[182:185], v[102:105], v[46:49]
	v_mfma_f32_16x16x32_f16 v[42:45], v[182:185], v[110:113], v[42:45]
	v_mfma_f32_16x16x32_f16 v[38:41], v[182:185], v[150:153], v[38:41]
	s_waitcnt lgkmcnt(0)
	v_mfma_f32_16x16x32_f16 v[34:37], v[190:193], v[102:105], v[34:37]
	v_mfma_f32_16x16x32_f16 v[30:33], v[190:193], v[110:113], v[30:33]
	v_mfma_f32_16x16x32_f16 v[26:29], v[190:193], v[150:153], v[26:29]
	s_setprio 0
	s_setprio 1
	v_mfma_f32_16x16x32_f16 v[22:25], v[178:181], v[154:157], v[22:25]
	v_mfma_f32_16x16x32_f16 v[18:21], v[178:181], v[162:165], v[18:21]
	v_mfma_f32_16x16x32_f16 v[14:17], v[178:181], v[170:173], v[14:17]
	v_mfma_f32_16x16x32_f16 v[10:13], v[186:189], v[154:157], v[10:13]
	v_mfma_f32_16x16x32_f16 v[6:9], v[186:189], v[162:165], v[6:9]
	v_mfma_f32_16x16x32_f16 v[2:5], v[186:189], v[170:173], v[2:5]
	v_mfma_f32_16x16x32_f16 v[22:25], v[182:185], v[158:161], v[22:25]
	v_mfma_f32_16x16x32_f16 v[18:21], v[182:185], v[166:169], v[18:21]
	v_mfma_f32_16x16x32_f16 v[14:17], v[182:185], v[174:177], v[14:17]
	v_mfma_f32_16x16x32_f16 v[10:13], v[190:193], v[158:161], v[10:13]
	v_mfma_f32_16x16x32_f16 v[6:9], v[190:193], v[166:169], v[6:9]
	v_mfma_f32_16x16x32_f16 v[2:5], v[190:193], v[174:177], v[2:5]
	s_setprio 0
	s_barrier
	ds_read_b128 v[178:181], v138 offset:16384
	ds_read_b128 v[182:185], v138 offset:17408
	ds_read_b128 v[186:189], v138 offset:18432
	ds_read_b128 v[190:193], v139 offset:19456
	s_waitcnt vmcnt(2)
	s_waitcnt lgkmcnt(0)
	s_barrier
	s_setprio 1
	s_waitcnt lgkmcnt(3)
	v_mfma_f32_16x16x32_f16 v[94:97], v[178:181], v[98:101], v[94:97]
	v_mfma_f32_16x16x32_f16 v[90:93], v[178:181], v[106:109], v[90:93]
	v_mfma_f32_16x16x32_f16 v[86:89], v[178:181], v[146:149], v[86:89]
	s_waitcnt lgkmcnt(1)
	v_mfma_f32_16x16x32_f16 v[82:85], v[186:189], v[98:101], v[82:85]
	v_mfma_f32_16x16x32_f16 v[78:81], v[186:189], v[106:109], v[78:81]
	v_mfma_f32_16x16x32_f16 v[74:77], v[186:189], v[146:149], v[74:77]
	v_mfma_f32_16x16x32_f16 v[194:197], v[182:185], v[102:105], v[94:97]
	v_mfma_f32_16x16x32_f16 v[198:201], v[182:185], v[110:113], v[90:93]
	v_mfma_f32_16x16x32_f16 v[202:205], v[182:185], v[150:153], v[86:89]
	s_waitcnt lgkmcnt(0)
	v_mfma_f32_16x16x32_f16 v[206:209], v[190:193], v[102:105], v[82:85]
	v_mfma_f32_16x16x32_f16 v[106:109], v[190:193], v[110:113], v[78:81]
	v_mfma_f32_16x16x32_f16 v[110:113], v[190:193], v[150:153], v[74:77]
	s_setprio 0
	s_setprio 1
	v_mfma_f32_16x16x32_f16 v[70:73], v[178:181], v[154:157], v[70:73]
	v_mfma_f32_16x16x32_f16 v[66:69], v[178:181], v[162:165], v[66:69]
	v_mfma_f32_16x16x32_f16 v[62:65], v[178:181], v[170:173], v[62:65]
	v_mfma_f32_16x16x32_f16 v[58:61], v[186:189], v[154:157], v[58:61]
	v_mfma_f32_16x16x32_f16 v[54:57], v[186:189], v[162:165], v[54:57]
	v_mfma_f32_16x16x32_f16 v[50:53], v[186:189], v[170:173], v[50:53]
	v_mfma_f32_16x16x32_f16 v[146:149], v[182:185], v[158:161], v[70:73]
	v_mfma_f32_16x16x32_f16 v[150:153], v[182:185], v[166:169], v[66:69]
	v_mfma_f32_16x16x32_f16 v[178:181], v[182:185], v[174:177], v[62:65]
	v_mfma_f32_16x16x32_f16 v[154:157], v[190:193], v[158:161], v[58:61]
	v_mfma_f32_16x16x32_f16 v[54:57], v[190:193], v[166:169], v[54:57]
	v_mfma_f32_16x16x32_f16 v[50:53], v[190:193], v[174:177], v[50:53]
	s_setprio 0
	s_barrier
	ds_read_b128 v[158:161], v140
	ds_read_b128 v[162:165], v140 offset:1024
	ds_read_b128 v[166:169], v141
	ds_read_b128 v[170:173], v141 offset:1024
	ds_read_b128 v[174:177], v142
	ds_read_b128 v[182:185], v142 offset:1024
	ds_read_b128 v[186:189], v143
	ds_read_b128 v[190:193], v143 offset:1024
	ds_read_b128 v[210:213], v144
	ds_read_b128 v[214:217], v144 offset:1024
	ds_read_b128 v[218:221], v145
	ds_read_b128 v[222:225], v145 offset:1024
	ds_read_b128 v[66:69], v138 offset:32768
	ds_read_b128 v[74:77], v138 offset:33792
	ds_read_b128 v[226:229], v138 offset:34816
	ds_read_b128 v[230:233], v139 offset:35840
	s_waitcnt vmcnt(0)
	s_waitcnt lgkmcnt(0)
	s_barrier
	s_setprio 1
	s_waitcnt lgkmcnt(3)
	v_mfma_f32_16x16x32_f16 v[46:49], v[66:69], v[158:161], v[46:49]
	v_mfma_f32_16x16x32_f16 v[42:45], v[66:69], v[166:169], v[42:45]
	v_mfma_f32_16x16x32_f16 v[38:41], v[66:69], v[174:177], v[38:41]
	s_waitcnt lgkmcnt(1)
	v_mfma_f32_16x16x32_f16 v[34:37], v[226:229], v[158:161], v[34:37]
	v_mfma_f32_16x16x32_f16 v[30:33], v[226:229], v[166:169], v[30:33]
	v_mfma_f32_16x16x32_f16 v[26:29], v[226:229], v[174:177], v[26:29]
	v_mfma_f32_16x16x32_f16 v[94:97], v[74:77], v[162:165], v[46:49]
	v_mfma_f32_16x16x32_f16 v[86:89], v[74:77], v[170:173], v[42:45]
	v_mfma_f32_16x16x32_f16 v[82:85], v[74:77], v[182:185], v[38:41]
	s_waitcnt lgkmcnt(0)
	v_mfma_f32_16x16x32_f16 v[70:73], v[230:233], v[162:165], v[34:37]
	v_mfma_f32_16x16x32_f16 v[62:65], v[230:233], v[170:173], v[30:33]
	v_mfma_f32_16x16x32_f16 v[58:61], v[230:233], v[182:185], v[26:29]
	s_setprio 0
	s_setprio 1
	v_mfma_f32_16x16x32_f16 v[22:25], v[66:69], v[186:189], v[22:25]
	v_mfma_f32_16x16x32_f16 v[18:21], v[66:69], v[210:213], v[18:21]
	v_mfma_f32_16x16x32_f16 v[14:17], v[66:69], v[218:221], v[14:17]
	v_mfma_f32_16x16x32_f16 v[10:13], v[226:229], v[186:189], v[10:13]
	v_mfma_f32_16x16x32_f16 v[6:9], v[226:229], v[210:213], v[6:9]
	v_mfma_f32_16x16x32_f16 v[2:5], v[226:229], v[218:221], v[2:5]
	v_mfma_f32_16x16x32_f16 v[102:105], v[74:77], v[190:193], v[22:25]
	v_mfma_f32_16x16x32_f16 v[98:101], v[74:77], v[214:217], v[18:21]
	v_mfma_f32_16x16x32_f16 v[90:93], v[74:77], v[222:225], v[14:17]
	v_mfma_f32_16x16x32_f16 v[78:81], v[230:233], v[190:193], v[10:13]
	v_mfma_f32_16x16x32_f16 v[74:77], v[230:233], v[214:217], v[6:9]
	v_mfma_f32_16x16x32_f16 v[66:69], v[230:233], v[222:225], v[2:5]
	s_setprio 0
	s_barrier
	ds_read_b128 v[10:13], v138 offset:49152
	ds_read_b128 v[18:21], v138 offset:50176
	ds_read_b128 v[226:229], v138 offset:51200
	ds_read_b128 v[230:233], v139 offset:52224
	s_waitcnt lgkmcnt(0)
	s_barrier
	s_setprio 1
	s_waitcnt lgkmcnt(3)
	v_mfma_f32_16x16x32_f16 v[2:5], v[10:13], v[158:161], v[194:197]
	s_waitcnt lgkmcnt(2)
	v_mfma_f32_16x16x32_f16 v[38:41], v[18:21], v[162:165], v[2:5]
	v_mfma_f32_16x16x32_f16 v[2:5], v[10:13], v[166:169], v[198:201]
	v_mfma_f32_16x16x32_f16 v[30:33], v[18:21], v[170:173], v[2:5]
	v_mfma_f32_16x16x32_f16 v[2:5], v[10:13], v[174:177], v[202:205]
	v_mfma_f32_16x16x32_f16 v[26:29], v[18:21], v[182:185], v[2:5]
	s_waitcnt lgkmcnt(1)
	v_mfma_f32_16x16x32_f16 v[2:5], v[226:229], v[158:161], v[206:209]
	s_waitcnt lgkmcnt(0)
	v_mfma_f32_16x16x32_f16 v[14:17], v[230:233], v[162:165], v[2:5]
	v_mfma_f32_16x16x32_f16 v[2:5], v[226:229], v[166:169], v[106:109]
	v_mfma_f32_16x16x32_f16 v[6:9], v[230:233], v[170:173], v[2:5]
	v_mfma_f32_16x16x32_f16 v[2:5], v[226:229], v[174:177], v[110:113]
	v_mfma_f32_16x16x32_f16 v[2:5], v[230:233], v[182:185], v[2:5]
	s_setprio 0
	s_setprio 1
	v_mfma_f32_16x16x32_f16 v[22:25], v[10:13], v[186:189], v[146:149]
	v_mfma_f32_16x16x32_f16 v[46:49], v[18:21], v[190:193], v[22:25]
	v_mfma_f32_16x16x32_f16 v[22:25], v[10:13], v[210:213], v[150:153]
	v_mfma_f32_16x16x32_f16 v[10:13], v[10:13], v[218:221], v[178:181]
	v_mfma_f32_16x16x32_f16 v[34:37], v[18:21], v[222:225], v[10:13]
	v_mfma_f32_16x16x32_f16 v[10:13], v[226:229], v[186:189], v[154:157]
	v_mfma_f32_16x16x32_f16 v[42:45], v[18:21], v[214:217], v[22:25]
	v_mfma_f32_16x16x32_f16 v[22:25], v[230:233], v[190:193], v[10:13]
	v_mfma_f32_16x16x32_f16 v[10:13], v[226:229], v[210:213], v[54:57]
	v_mfma_f32_16x16x32_f16 v[18:21], v[230:233], v[214:217], v[10:13]
	v_mfma_f32_16x16x32_f16 v[10:13], v[226:229], v[218:221], v[50:53]
	v_mfma_f32_16x16x32_f16 v[10:13], v[230:233], v[222:225], v[10:13]
	s_setprio 0
	s_barrier
	s_and_saveexec_b64 s[0:1], s[4:5]
	s_cbranch_execz .LBB5_10
	s_barrier
.LBB5_10:
	s_or_b64 exec, exec, s[0:1]
	v_mov_b32_e32 v147, v0
	s_add_i32 s24, s24, s27
	v_ashrrev_i32_e32 v50, 2, v147
	v_and_b32_e32 v146, 0xffffffe0, v50
	v_lshrrev_b32_e32 v50, 2, v147
	v_add_u32_e32 v151, s29, v146
	v_and_b32_e32 v148, 12, v50
	v_or_b32_e32 v54, v151, v148
	v_or_b32_e32 v52, 16, v54
	v_min_i32_e32 v50, 0x2edc, v54
	v_min_i32_e32 v52, 0x2edc, v52
	v_ashrrev_i32_e32 v51, 31, v50
	v_ashrrev_i32_e32 v53, 31, v52
	v_lshl_add_u64 v[50:51], v[50:51], 2, s[10:11]
	v_lshl_add_u64 v[52:53], v[52:53], 2, s[10:11]
	global_load_dwordx4 v[110:113], v[50:51], off
	global_load_dwordx4 v[106:109], v[52:53], off
	v_add_u32_e32 v50, 0x80, v54
	v_add_u32_e32 v52, 0x90, v54
	v_min_i32_e32 v50, 0x2edc, v50
	v_min_i32_e32 v52, 0x2edc, v52
	v_ashrrev_i32_e32 v51, 31, v50
	v_ashrrev_i32_e32 v53, 31, v52
	v_lshl_add_u64 v[50:51], v[50:51], 2, s[10:11]
	v_lshl_add_u64 v[52:53], v[52:53], 2, s[10:11]
	global_load_dwordx4 v[54:57], v[50:51], off
	s_nop 0
	global_load_dwordx4 v[50:53], v[52:53], off
	s_cmpk_lt_u32 s24, 0x5e
	s_cselect_b64 s[0:1], -1, 0
	s_cmpk_gt_u32 s24, 0x5d
	s_mov_b32 s33, s31
	s_waitcnt vmcnt(0)
	s_cbranch_scc1 .LBB5_12
	s_add_i32 s6, s24, s25
	s_lshr_b32 s7, s6, 4
	s_and_b32 s29, s7, 0x78
	s_sub_i32 s7, 47, s29
	s_min_u32 s33, s7, 8
	v_cvt_f32_ubyte0_e32 v149, s33
	v_rcp_iflag_f32_e32 v150, v149
	s_and_b32 s34, s6, 0x7f
	v_cvt_f32_ubyte0_e32 v152, s34
	v_readfirstlane_b32 s35, v120
	v_mul_f32_e32 v150, v152, v150
	v_trunc_f32_e32 v150, v150
	v_cvt_u32_f32_e32 v153, v150
	v_fma_f32 v150, -v150, v149, v152
	v_cmp_ge_f32_e64 s[6:7], |v150|, v149
	s_cmp_lg_u64 s[6:7], 0
	v_readfirstlane_b32 s6, v153
	s_addc_u32 s6, s6, 0
	s_mul_i32 s7, s6, s33
	s_sub_i32 s7, s34, s7
	s_and_b32 s6, s6, 0xff
	s_and_b32 s7, s7, 0xff
	v_readfirstlane_b32 s33, v115
	s_add_i32 s29, s29, s7
	s_mul_i32 s7, s6, 0x60000
	s_mov_b32 m0, s33
	v_readfirstlane_b32 s33, v117
	buffer_load_dwordx4 v1, s[16:19], s7 offen lds
	s_mov_b32 m0, s33
	v_readfirstlane_b32 s34, v118
	buffer_load_dwordx4 v116, s[16:19], s7 offen lds
	s_lshl_b32 s33, s29, 19
	s_mov_b32 m0, s34
	v_readfirstlane_b32 s34, v119
	buffer_load_dwordx4 v1, s[12:15], s33 offen lds
	s_mov_b32 m0, s34
	s_add_i32 s34, s7, 0x30000
	buffer_load_dwordx4 v114, s[12:15], s33 offen lds
	s_mov_b32 m0, s35
	v_readfirstlane_b32 s35, v121
	buffer_load_dwordx4 v1, s[16:19], s34 offen lds
	s_mov_b32 m0, s35
	v_readfirstlane_b32 s35, v122
	buffer_load_dwordx4 v116, s[16:19], s34 offen lds
	s_or_b32 s34, s33, 0x40000
	s_mov_b32 m0, s35
	v_readfirstlane_b32 s35, v123
	buffer_load_dwordx4 v1, s[12:15], s34 offen lds
	s_mov_b32 m0, s35
	v_readfirstlane_b32 s35, v124
	buffer_load_dwordx4 v114, s[12:15], s34 offen lds
	s_or_b32 s34, s7, 0x80
	s_mov_b32 m0, s35
	v_readfirstlane_b32 s35, v125
	buffer_load_dwordx4 v1, s[16:19], s34 offen lds
	s_mov_b32 m0, s35
	s_bitset1_b32 s33, 7
	buffer_load_dwordx4 v116, s[16:19], s34 offen lds
	v_readfirstlane_b32 s34, v126
	s_mov_b32 m0, s34
	v_readfirstlane_b32 s34, v127
	buffer_load_dwordx4 v1, s[12:15], s33 offen lds
	s_mov_b32 m0, s34
	s_add_i32 s7, s7, 0x30080
	buffer_load_dwordx4 v114, s[12:15], s33 offen lds
	v_readfirstlane_b32 s33, v128
	s_mov_b32 m0, s33
	v_readfirstlane_b32 s33, v129
	buffer_load_dwordx4 v1, s[16:19], s7 offen lds
	s_mov_b32 m0, s33
	s_lshl_b32 s29, s29, 8
	buffer_load_dwordx4 v116, s[16:19], s7 offen lds
	s_mul_i32 s33, s6, 0xc0

.LBB5_15:
	v_add_f32_e32 v94, v110, v94
	v_add_f32_e32 v160, v110, v82
	v_add_f32_e32 v70, v106, v70
	v_mov_b32_e32 v82, v94
	s_ashr_i32 s34, s31, 7
	v_add_f32_e32 v95, v95, v111
	v_add_f32_e32 v96, v96, v112
	v_add_f32_e32 v97, v97, v113
	v_mov_b32_dpp v82, v70 row_ror:8 row_mask:0xf bank_mask:0xc
	v_mov_b32_dpp v70, v94 row_ror:8 row_mask:0xf bank_mask:0x3
	v_mad_u32_u24 v94, v158, 24, s34
	v_add_f32_e32 v161, v83, v111
	v_add_f32_e32 v162, v84, v112
	v_add_f32_e32 v163, v85, v113
	v_add_f32_e32 v71, v71, v107
	v_add_f32_e32 v72, v72, v108
	v_add_f32_e32 v73, v73, v109
	v_add_f32_e32 v62, v106, v62
	v_add_f32_e32 v58, v106, v58
	v_add_f32_e32 v78, v106, v78
	v_add_f32_e32 v74, v106, v74
	v_add_f32_e32 v66, v106, v66
	v_or_b32_e32 v106, v151, v159
	v_mov_b32_e32 v83, v95
	v_mov_b32_e32 v84, v96
	v_mov_b32_e32 v85, v97
	s_addk_i32 s34, 0xc0
	v_mul_lo_u32 v94, v94, s8
	v_mov_b32_dpp v83, v71 row_ror:8 row_mask:0xf bank_mask:0xc
	v_mov_b32_dpp v84, v72 row_ror:8 row_mask:0xf bank_mask:0xc
	v_mov_b32_dpp v85, v73 row_ror:8 row_mask:0xf bank_mask:0xc
	v_mov_b32_dpp v71, v95 row_ror:8 row_mask:0xf bank_mask:0x3
	v_mad_u32_u24 v95, v158, 24, s34
	v_add_lshl_u32 v94, v94, v106, 2
	buffer_store_dwordx4 v[82:85], v94, s[20:23], 0 offen sc1
	v_mov_b32_dpp v72, v96 row_ror:8 row_mask:0xf bank_mask:0x3
	v_mov_b32_dpp v73, v97 row_ror:8 row_mask:0xf bank_mask:0x3
	v_mul_lo_u32 v82, v95, s8
	v_add_lshl_u32 v82, v82, v106, 2
	v_add_f32_e32 v86, v110, v86
	v_add_f32_e32 v87, v87, v111
	v_add_f32_e32 v88, v88, v112
	v_add_f32_e32 v89, v89, v113
	buffer_store_dwordx4 v[70:73], v82, s[20:23], 0 offen sc1
	v_mad_u32_u24 v82, v156, 24, v157
	v_add_f32_e32 v63, v63, v107
	v_add_f32_e32 v64, v64, v108
	v_add_f32_e32 v65, v65, v109
	v_mov_b32_e32 v70, v86
	v_mov_b32_e32 v71, v87
	v_mov_b32_e32 v72, v88
	v_mov_b32_e32 v73, v89
	v_mul_lo_u32 v82, v82, s8
	v_mov_b32_dpp v70, v62 row_ror:8 row_mask:0xf bank_mask:0xc
	v_mov_b32_dpp v71, v63 row_ror:8 row_mask:0xf bank_mask:0xc
	v_mov_b32_dpp v72, v64 row_ror:8 row_mask:0xf bank_mask:0xc
	v_mov_b32_dpp v73, v65 row_ror:8 row_mask:0xf bank_mask:0xc
	v_add_lshl_u32 v82, v82, v106, 2
	v_mov_b32_dpp v62, v86 row_ror:8 row_mask:0xf bank_mask:0x3
	v_mov_b32_dpp v63, v87 row_ror:8 row_mask:0xf bank_mask:0x3
	v_mov_b32_dpp v64, v88 row_ror:8 row_mask:0xf bank_mask:0x3
	v_mov_b32_dpp v65, v89 row_ror:8 row_mask:0xf bank_mask:0x3
	buffer_store_dwordx4 v[70:73], v82, s[20:23], 0 offen sc1
	v_add_f32_e32 v59, v59, v107
	v_add_f32_e32 v60, v60, v108
	v_add_u32_e32 v70, 0x8ca000, v82
	buffer_store_dwordx4 v[62:65], v70, s[20:23], 0 offen sc1
	v_mad_u32_u24 v70, v154, 24, v155
	v_add_f32_e32 v61, v61, v109
	v_mov_b32_e32 v62, v160
	v_mov_b32_e32 v63, v161
	v_mov_b32_e32 v64, v162
	v_mov_b32_e32 v65, v163
	v_mul_lo_u32 v70, v70, s8
	v_mov_b32_dpp v62, v58 row_ror:8 row_mask:0xf bank_mask:0xc
	v_mov_b32_dpp v63, v59 row_ror:8 row_mask:0xf bank_mask:0xc
	v_mov_b32_dpp v64, v60 row_ror:8 row_mask:0xf bank_mask:0xc
	v_mov_b32_dpp v65, v61 row_ror:8 row_mask:0xf bank_mask:0xc
	v_add_lshl_u32 v70, v70, v106, 2
	v_mov_b32_dpp v58, v160 row_ror:8 row_mask:0xf bank_mask:0x3
	v_mov_b32_dpp v59, v161 row_ror:8 row_mask:0xf bank_mask:0x3
	v_mov_b32_dpp v60, v162 row_ror:8 row_mask:0xf bank_mask:0x3
	v_mov_b32_dpp v61, v163 row_ror:8 row_mask:0xf bank_mask:0x3
	buffer_store_dwordx4 v[62:65], v70, s[20:23], 0 offen sc1
	v_add_f32_e32 v102, v110, v102
	v_add_f32_e32 v103, v103, v111
	v_add_u32_e32 v62, 0x8ca000, v70
	v_add_f32_e32 v104, v104, v112
	v_add_f32_e32 v105, v105, v113
	buffer_store_dwordx4 v[58:61], v62, s[20:23], 0 offen sc1
	v_mad_u32_u24 v62, v152, 24, v153
	v_add_f32_e32 v79, v79, v107
	v_add_f32_e32 v80, v80, v108
	v_add_f32_e32 v81, v81, v109
	v_mov_b32_e32 v58, v102
	v_mov_b32_e32 v59, v103
	v_mov_b32_e32 v60, v104
	v_mov_b32_e32 v61, v105
	v_mul_lo_u32 v62, v62, s8
	v_mov_b32_dpp v58, v78 row_ror:8 row_mask:0xf bank_mask:0xc
	v_mov_b32_dpp v59, v79 row_ror:8 row_mask:0xf bank_mask:0xc
	v_mov_b32_dpp v60, v80 row_ror:8 row_mask:0xf bank_mask:0xc
	v_mov_b32_dpp v61, v81 row_ror:8 row_mask:0xf bank_mask:0xc
	v_add_lshl_u32 v62, v62, v106, 2
	v_add_f32_e32 v98, v110, v98
	v_add_f32_e32 v99, v99, v111
	v_add_f32_e32 v100, v100, v112
	v_add_f32_e32 v101, v101, v113
	v_mov_b32_dpp v78, v102 row_ror:8 row_mask:0xf bank_mask:0x3
	v_mov_b32_dpp v79, v103 row_ror:8 row_mask:0xf bank_mask:0x3
	v_mov_b32_dpp v80, v104 row_ror:8 row_mask:0xf bank_mask:0x3
	v_mov_b32_dpp v81, v105 row_ror:8 row_mask:0xf bank_mask:0x3
	buffer_store_dwordx4 v[58:61], v62, s[20:23], 0 offen sc1
	v_add_f32_e32 v75, v75, v107
	v_add_f32_e32 v76, v76, v108
	v_add_u32_e32 v58, 0x8ca000, v62
	v_mad_u32_u24 v62, v149, 24, v150
	v_add_f32_e32 v77, v77, v109
	buffer_store_dwordx4 v[78:81], v58, s[20:23], 0 offen sc1
	v_mov_b32_e32 v58, v98
	v_mov_b32_e32 v59, v99
	v_mov_b32_e32 v60, v100
	v_mov_b32_e32 v61, v101
	v_mul_lo_u32 v62, v62, s8
	v_mov_b32_dpp v58, v74 row_ror:8 row_mask:0xf bank_mask:0xc
	v_mov_b32_dpp v59, v75 row_ror:8 row_mask:0xf bank_mask:0xc
	v_mov_b32_dpp v60, v76 row_ror:8 row_mask:0xf bank_mask:0xc
	v_mov_b32_dpp v61, v77 row_ror:8 row_mask:0xf bank_mask:0xc
	v_add_lshl_u32 v62, v62, v106, 2
	v_add_f32_e32 v90, v110, v90
	v_add_f32_e32 v91, v91, v111
	v_add_f32_e32 v92, v92, v112
	v_add_f32_e32 v93, v93, v113
	v_mov_b32_dpp v74, v98 row_ror:8 row_mask:0xf bank_mask:0x3
	v_mov_b32_dpp v75, v99 row_ror:8 row_mask:0xf bank_mask:0x3
	v_mov_b32_dpp v76, v100 row_ror:8 row_mask:0xf bank_mask:0x3
	v_mov_b32_dpp v77, v101 row_ror:8 row_mask:0xf bank_mask:0x3
	buffer_store_dwordx4 v[58:61], v62, s[20:23], 0 offen sc1
	v_add_f32_e32 v67, v67, v107
	v_add_f32_e32 v68, v68, v108
	v_add_u32_e32 v58, 0x8ca000, v62
	v_mad_u32_u24 v62, v147, 24, v148
	v_add_f32_e32 v69, v69, v109
	buffer_store_dwordx4 v[74:77], v58, s[20:23], 0 offen sc1
	v_mov_b32_e32 v58, v90
	v_mov_b32_e32 v59, v91
	v_mov_b32_e32 v60, v92
	v_mov_b32_e32 v61, v93
	v_mul_lo_u32 v62, v62, s8
	v_mov_b32_dpp v58, v66 row_ror:8 row_mask:0xf bank_mask:0xc
	v_mov_b32_dpp v59, v67 row_ror:8 row_mask:0xf bank_mask:0xc
	v_mov_b32_dpp v60, v68 row_ror:8 row_mask:0xf bank_mask:0xc
	v_mov_b32_dpp v61, v69 row_ror:8 row_mask:0xf bank_mask:0xc
	v_add_lshl_u32 v62, v62, v106, 2
	v_mov_b32_dpp v66, v90 row_ror:8 row_mask:0xf bank_mask:0x3
	v_mov_b32_dpp v67, v91 row_ror:8 row_mask:0xf bank_mask:0x3
	v_mov_b32_dpp v68, v92 row_ror:8 row_mask:0xf bank_mask:0x3
	v_mov_b32_dpp v69, v93 row_ror:8 row_mask:0xf bank_mask:0x3
	buffer_store_dwordx4 v[58:61], v62, s[20:23], 0 offen sc1
	s_nop 1
	v_add_u32_e32 v58, 0x8ca000, v62
	buffer_store_dwordx4 v[66:69], v58, s[20:23], 0 offen sc1
	s_or_b64 exec, exec, s[6:7]
	v_cmp_gt_i32_e32 vcc, s28, v151
	s_and_saveexec_b64 s[6:7], vcc
	s_cbranch_execz .LBB5_14
.LBB5_16:
	v_add_f32_e32 v38, v54, v38
	v_add_f32_e32 v58, v54, v26
	v_add_f32_e32 v14, v50, v14
	v_mov_b32_e32 v26, v38
	s_ashr_i32 s31, s31, 7
	v_add_f32_e32 v39, v39, v55
	v_add_f32_e32 v40, v40, v56
	v_add_f32_e32 v41, v41, v57
	v_mov_b32_dpp v26, v14 row_ror:8 row_mask:0xf bank_mask:0xc
	v_mov_b32_dpp v14, v38 row_ror:8 row_mask:0xf bank_mask:0x3
	v_mad_u32_u24 v38, v158, 24, s31
	v_add_f32_e32 v59, v27, v55
	v_add_f32_e32 v60, v28, v56
	v_add_f32_e32 v61, v29, v57
	v_add_f32_e32 v15, v15, v51
	v_add_f32_e32 v16, v16, v52
	v_add_f32_e32 v17, v17, v53
	v_add_f32_e32 v6, v50, v6
	v_add_f32_e32 v2, v50, v2
	v_add_f32_e32 v22, v50, v22
	v_add_f32_e32 v18, v50, v18
	v_add_f32_e32 v10, v50, v10
	v_add3_u32 v50, v151, v159, s26
	v_mov_b32_e32 v27, v39
	v_mov_b32_e32 v28, v40
	v_mov_b32_e32 v29, v41
	s_addk_i32 s31, 0xc0
	v_mul_lo_u32 v38, v38, s8
	v_mov_b32_dpp v27, v15 row_ror:8 row_mask:0xf bank_mask:0xc
	v_mov_b32_dpp v28, v16 row_ror:8 row_mask:0xf bank_mask:0xc
	v_mov_b32_dpp v29, v17 row_ror:8 row_mask:0xf bank_mask:0xc
	v_mov_b32_dpp v15, v39 row_ror:8 row_mask:0xf bank_mask:0x3
	v_mad_u32_u24 v39, v158, 24, s31
	v_add_lshl_u32 v38, v38, v50, 2
	buffer_store_dwordx4 v[26:29], v38, s[20:23], 0 offen sc1
	v_mov_b32_dpp v16, v40 row_ror:8 row_mask:0xf bank_mask:0x3
	v_mov_b32_dpp v17, v41 row_ror:8 row_mask:0xf bank_mask:0x3
	v_mul_lo_u32 v26, v39, s8
	v_add_lshl_u32 v26, v26, v50, 2
	v_add_f32_e32 v30, v54, v30
	v_add_f32_e32 v31, v31, v55
	v_add_f32_e32 v32, v32, v56
	v_add_f32_e32 v33, v33, v57
	buffer_store_dwordx4 v[14:17], v26, s[20:23], 0 offen sc1
	v_mad_u32_u24 v26, v156, 24, v157
	v_add_f32_e32 v7, v7, v51
	v_add_f32_e32 v8, v8, v52
	v_add_f32_e32 v9, v9, v53
	v_mov_b32_e32 v14, v30
	v_mov_b32_e32 v15, v31
	v_mov_b32_e32 v16, v32
	v_mov_b32_e32 v17, v33
	v_mul_lo_u32 v26, v26, s8
	v_mov_b32_dpp v14, v6 row_ror:8 row_mask:0xf bank_mask:0xc
	v_mov_b32_dpp v15, v7 row_ror:8 row_mask:0xf bank_mask:0xc
	v_mov_b32_dpp v16, v8 row_ror:8 row_mask:0xf bank_mask:0xc
	v_mov_b32_dpp v17, v9 row_ror:8 row_mask:0xf bank_mask:0xc
	v_add_lshl_u32 v26, v26, v50, 2
	v_mov_b32_dpp v6, v30 row_ror:8 row_mask:0xf bank_mask:0x3
	v_mov_b32_dpp v7, v31 row_ror:8 row_mask:0xf bank_mask:0x3
	v_mov_b32_dpp v8, v32 row_ror:8 row_mask:0xf bank_mask:0x3
	v_mov_b32_dpp v9, v33 row_ror:8 row_mask:0xf bank_mask:0x3
	buffer_store_dwordx4 v[14:17], v26, s[20:23], 0 offen sc1
	v_add_f32_e32 v3, v3, v51
	v_add_f32_e32 v4, v4, v52
	v_add_u32_e32 v14, 0x8ca000, v26
	buffer_store_dwordx4 v[6:9], v14, s[20:23], 0 offen sc1
	v_mad_u32_u24 v14, v154, 24, v155
	v_add_f32_e32 v5, v5, v53
	v_mov_b32_e32 v6, v58
	v_mov_b32_e32 v7, v59
	v_mov_b32_e32 v8, v60
	v_mov_b32_e32 v9, v61
	v_mul_lo_u32 v14, v14, s8
	v_mov_b32_dpp v6, v2 row_ror:8 row_mask:0xf bank_mask:0xc
	v_mov_b32_dpp v7, v3 row_ror:8 row_mask:0xf bank_mask:0xc
	v_mov_b32_dpp v8, v4 row_ror:8 row_mask:0xf bank_mask:0xc
	v_mov_b32_dpp v9, v5 row_ror:8 row_mask:0xf bank_mask:0xc
	v_add_lshl_u32 v14, v14, v50, 2
	v_mov_b32_dpp v2, v58 row_ror:8 row_mask:0xf bank_mask:0x3
	v_mov_b32_dpp v3, v59 row_ror:8 row_mask:0xf bank_mask:0x3
	v_mov_b32_dpp v4, v60 row_ror:8 row_mask:0xf bank_mask:0x3
	v_mov_b32_dpp v5, v61 row_ror:8 row_mask:0xf bank_mask:0x3
	buffer_store_dwordx4 v[6:9], v14, s[20:23], 0 offen sc1
	v_add_f32_e32 v46, v54, v46
	v_add_f32_e32 v47, v47, v55
	v_add_u32_e32 v6, 0x8ca000, v14
	v_add_f32_e32 v48, v48, v56
	v_add_f32_e32 v49, v49, v57
	buffer_store_dwordx4 v[2:5], v6, s[20:23], 0 offen sc1
	v_mad_u32_u24 v6, v152, 24, v153
	v_add_f32_e32 v23, v23, v51
	v_add_f32_e32 v24, v24, v52
	v_add_f32_e32 v25, v25, v53
	v_mov_b32_e32 v2, v46
	v_mov_b32_e32 v3, v47
	v_mov_b32_e32 v4, v48
	v_mov_b32_e32 v5, v49
	v_mul_lo_u32 v6, v6, s8
	v_mov_b32_dpp v2, v22 row_ror:8 row_mask:0xf bank_mask:0xc
	v_mov_b32_dpp v3, v23 row_ror:8 row_mask:0xf bank_mask:0xc
	v_mov_b32_dpp v4, v24 row_ror:8 row_mask:0xf bank_mask:0xc
	v_mov_b32_dpp v5, v25 row_ror:8 row_mask:0xf bank_mask:0xc
	v_add_lshl_u32 v6, v6, v50, 2
	v_add_f32_e32 v42, v54, v42
	v_add_f32_e32 v43, v43, v55
	v_add_f32_e32 v44, v44, v56
	v_add_f32_e32 v45, v45, v57
	v_mov_b32_dpp v22, v46 row_ror:8 row_mask:0xf bank_mask:0x3
	v_mov_b32_dpp v23, v47 row_ror:8 row_mask:0xf bank_mask:0x3
	v_mov_b32_dpp v24, v48 row_ror:8 row_mask:0xf bank_mask:0x3
	v_mov_b32_dpp v25, v49 row_ror:8 row_mask:0xf bank_mask:0x3
	buffer_store_dwordx4 v[2:5], v6, s[20:23], 0 offen sc1
	v_add_f32_e32 v19, v19, v51
	v_add_f32_e32 v20, v20, v52
	v_add_u32_e32 v2, 0x8ca000, v6
	v_mad_u32_u24 v6, v149, 24, v150
	v_add_f32_e32 v21, v21, v53
	buffer_store_dwordx4 v[22:25], v2, s[20:23], 0 offen sc1
	v_mov_b32_e32 v2, v42
	v_mov_b32_e32 v3, v43
	v_mov_b32_e32 v4, v44
	v_mov_b32_e32 v5, v45
	v_mul_lo_u32 v6, v6, s8
	v_mov_b32_dpp v2, v18 row_ror:8 row_mask:0xf bank_mask:0xc
	v_mov_b32_dpp v3, v19 row_ror:8 row_mask:0xf bank_mask:0xc
	v_mov_b32_dpp v4, v20 row_ror:8 row_mask:0xf bank_mask:0xc
	v_mov_b32_dpp v5, v21 row_ror:8 row_mask:0xf bank_mask:0xc
	v_add_lshl_u32 v6, v6, v50, 2
	v_add_f32_e32 v34, v54, v34
	v_add_f32_e32 v35, v35, v55
	v_add_f32_e32 v36, v36, v56
	v_add_f32_e32 v37, v37, v57
	v_mov_b32_dpp v18, v42 row_ror:8 row_mask:0xf bank_mask:0x3
	v_mov_b32_dpp v19, v43 row_ror:8 row_mask:0xf bank_mask:0x3
	v_mov_b32_dpp v20, v44 row_ror:8 row_mask:0xf bank_mask:0x3
	v_mov_b32_dpp v21, v45 row_ror:8 row_mask:0xf bank_mask:0x3
	buffer_store_dwordx4 v[2:5], v6, s[20:23], 0 offen sc1
	v_add_f32_e32 v11, v11, v51
	v_add_f32_e32 v12, v12, v52
	v_add_u32_e32 v2, 0x8ca000, v6
	v_mad_u32_u24 v6, v147, 24, v148
	v_add_f32_e32 v13, v13, v53
	buffer_store_dwordx4 v[18:21], v2, s[20:23], 0 offen sc1
	v_mov_b32_e32 v2, v34
	v_mov_b32_e32 v3, v35
	v_mov_b32_e32 v4, v36
	v_mov_b32_e32 v5, v37
	v_mul_lo_u32 v6, v6, s8
	v_mov_b32_dpp v2, v10 row_ror:8 row_mask:0xf bank_mask:0xc
	v_mov_b32_dpp v3, v11 row_ror:8 row_mask:0xf bank_mask:0xc
	v_mov_b32_dpp v4, v12 row_ror:8 row_mask:0xf bank_mask:0xc
	v_mov_b32_dpp v5, v13 row_ror:8 row_mask:0xf bank_mask:0xc
	v_add_lshl_u32 v6, v6, v50, 2
	v_mov_b32_dpp v10, v34 row_ror:8 row_mask:0xf bank_mask:0x3
	v_mov_b32_dpp v11, v35 row_ror:8 row_mask:0xf bank_mask:0x3
	v_mov_b32_dpp v12, v36 row_ror:8 row_mask:0xf bank_mask:0x3
	v_mov_b32_dpp v13, v37 row_ror:8 row_mask:0xf bank_mask:0x3
	buffer_store_dwordx4 v[2:5], v6, s[20:23], 0 offen sc1
	s_nop 1
	v_add_u32_e32 v2, 0x8ca000, v6
	buffer_store_dwordx4 v[10:13], v2, s[20:23], 0 offen sc1
	s_or_b64 exec, exec, s[6:7]
	s_andn2_b64 vcc, exec, s[0:1]
	s_mov_b64 s[0:1], -1
	s_cbranch_vccnz .LBB5_5

	.amdhsa_kernel _Z11gemm_8phaseILi1EEvPKDF16_S1_PfPKfS4_
		.amdhsa_group_segment_fixed_size 0
		.amdhsa_private_segment_fixed_size 0
		.amdhsa_kernarg_size 296
		.amdhsa_user_sgpr_count 2
		.amdhsa_user_sgpr_dispatch_ptr 0
		.amdhsa_user_sgpr_queue_ptr 0
		.amdhsa_user_sgpr_kernarg_segment_ptr 1
		.amdhsa_user_sgpr_dispatch_id 0
		.amdhsa_user_sgpr_kernarg_preload_length 0
		.amdhsa_user_sgpr_kernarg_preload_offset 0
		.amdhsa_user_sgpr_private_segment_size 0
		.amdhsa_uses_dynamic_stack 0
		.amdhsa_enable_private_segment 0
		.amdhsa_system_sgpr_workgroup_id_x 1
		.amdhsa_system_sgpr_workgroup_id_y 0
		.amdhsa_system_sgpr_workgroup_id_z 0
		.amdhsa_system_sgpr_workgroup_info 0
		.amdhsa_system_vgpr_workitem_id 0
		.amdhsa_next_free_vgpr 234
		.amdhsa_next_free_sgpr 38
		.amdhsa_accum_offset 236
		.amdhsa_reserve_vcc 1
		.amdhsa_float_round_mode_32 0
		.amdhsa_float_round_mode_16_64 0
		.amdhsa_float_denorm_mode_32 3
		.amdhsa_float_denorm_mode_16_64 3
		.amdhsa_dx10_clamp 1
		.amdhsa_ieee_mode 1
		.amdhsa_fp16_overflow 0
		.amdhsa_tg_split 0
		.amdhsa_exception_fp_ieee_invalid_op 0
		.amdhsa_exception_fp_denorm_src 0
		.amdhsa_exception_fp_ieee_div_zero 0
		.amdhsa_exception_fp_ieee_overflow 0
		.amdhsa_exception_fp_ieee_underflow 0
		.amdhsa_exception_fp_ieee_inexact 0
		.amdhsa_exception_int_div_zero 0
	.end_amdhsa_kernel

amdhsa.kernels:
  - .agpr_count:     0
    .args:
      - .actual_access:  read_only
        .address_space:  global
        .offset:         0
        .size:           8
        .value_kind:     global_buffer
      - .actual_access:  read_only
        .address_space:  global
        .offset:         8
        .size:           8
        .value_kind:     global_buffer
      - .actual_access:  read_only
        .address_space:  global
        .offset:         16
        .size:           8
        .value_kind:     global_buffer
      - .actual_access:  read_only
        .address_space:  global
        .offset:         24
        .size:           8
        .value_kind:     global_buffer
      - .actual_access:  read_only
        .address_space:  global
        .offset:         32
        .size:           8
        .value_kind:     global_buffer
      - .actual_access:  read_only
        .address_space:  global
        .offset:         40
        .size:           8
        .value_kind:     global_buffer
      - .address_space:  global
        .offset:         48
        .size:           8
        .value_kind:     global_buffer
      - .address_space:  global
        .offset:         56
        .size:           8
        .value_kind:     global_buffer
      - .address_space:  global
        .offset:         64
        .size:           8
        .value_kind:     global_buffer
      - .address_space:  global
        .offset:         72
        .size:           8
        .value_kind:     global_buffer
      - .address_space:  global
        .offset:         80
        .size:           8
        .value_kind:     global_buffer
    .group_segment_fixed_size: 0
    .kernarg_segment_align: 8
    .kernarg_segment_size: 88
    .language:       OpenCL C
    .language_version:
      - 2
      - 0
    .max_flat_workgroup_size: 256
    .name:           _Z11prep_kernelPKfPKiS0_S0_S0_S0_PDF16_S3_S3_S3_Pc
    .private_segment_fixed_size: 0
    .sgpr_count:     30
    .sgpr_spill_count: 0
    .symbol:         _Z11prep_kernelPKfPKiS0_S0_S0_S0_PDF16_S3_S3_S3_Pc.kd
    .uniform_work_group_size: 1
    .uses_dynamic_stack: false
    .vgpr_count:     14
    .vgpr_spill_count: 0
    .wavefront_size: 64
  - .agpr_count:     0
    .args:
      - .actual_access:  read_only
        .address_space:  global
        .offset:         0
        .size:           8
        .value_kind:     global_buffer
      - .address_space:  global
        .offset:         8
        .size:           8
        .value_kind:     global_buffer
    .group_segment_fixed_size: 0
    .kernarg_segment_align: 8
    .kernarg_segment_size: 16
    .language:       OpenCL C
    .language_version:
      - 2
      - 0
    .max_flat_workgroup_size: 256
    .name:           _Z7cvt_wfcPKfPDF16_
    .private_segment_fixed_size: 0
    .sgpr_count:     12
    .sgpr_spill_count: 0
    .symbol:         _Z7cvt_wfcPKfPDF16_.kd
    .uniform_work_group_size: 1
    .uses_dynamic_stack: false
    .vgpr_count:     12
    .vgpr_spill_count: 0
    .wavefront_size: 64
  - .agpr_count:     12
    .args:
      - .actual_access:  read_only
        .address_space:  global
        .offset:         0
        .size:           8
        .value_kind:     global_buffer
      - .actual_access:  read_only
        .address_space:  global
        .offset:         8
        .size:           8
        .value_kind:     global_buffer
      - .address_space:  global
        .offset:         16
        .size:           8
        .value_kind:     global_buffer
      - .address_space:  global
        .offset:         24
        .size:           8
        .value_kind:     global_buffer
      - .offset:         32
        .size:           4
        .value_kind:     by_value
    .group_segment_fixed_size: 0
    .kernarg_segment_align: 8
    .kernarg_segment_size: 36
    .language:       OpenCL C
    .language_version:
      - 2
      - 0
    .max_flat_workgroup_size: 256
    .name:           _Z9lstm_stepPKfS0_PDF16_Pfi
    .private_segment_fixed_size: 0
    .sgpr_count:     21
    .sgpr_spill_count: 0
    .symbol:         _Z9lstm_stepPKfS0_PDF16_Pfi.kd
    .uniform_work_group_size: 1
    .uses_dynamic_stack: false
    .vgpr_count:     88
    .vgpr_spill_count: 0
    .wavefront_size: 64
  - .agpr_count:     0
    .args:
      - .actual_access:  read_only
        .address_space:  global
        .offset:         0
        .size:           8
        .value_kind:     global_buffer
      - .actual_access:  read_only
        .address_space:  global
        .offset:         8
        .size:           8
        .value_kind:     global_buffer
      - .address_space:  global
        .offset:         16
        .size:           8
        .value_kind:     global_buffer
      - .address_space:  global
        .offset:         24
        .size:           8
        .value_kind:     global_buffer
      - .address_space:  global
        .offset:         32
        .size:           8
        .value_kind:     global_buffer
      - .actual_access:  read_only
        .address_space:  global
        .offset:         40
        .size:           8
        .value_kind:     global_buffer
      - .address_space:  global
        .offset:         48
        .size:           8
        .value_kind:     global_buffer
    .group_segment_fixed_size: 0
    .kernarg_segment_align: 8
    .kernarg_segment_size: 56
    .language:       OpenCL C
    .language_version:
      - 2
      - 0
    .max_flat_workgroup_size: 512
    .name:           _Z15lstm_persistentPKDF16_PKfPDF16_PjS4_S2_S3_
    .private_segment_fixed_size: 0
    .sgpr_count:     55
    .sgpr_spill_count: 0
    .symbol:         _Z15lstm_persistentPKDF16_PKfPDF16_PjS4_S2_S3_.kd
    .uniform_work_group_size: 1
    .uses_dynamic_stack: false
    .vgpr_count:     242
    .vgpr_spill_count: 0
    .wavefront_size: 64
  - .agpr_count:     0
    .args:
      - .address_space:  global
        .offset:         0
        .size:           8
        .value_kind:     global_buffer
      - .address_space:  global
        .offset:         8
        .size:           8
        .value_kind:     global_buffer
      - .address_space:  global
        .offset:         16
        .size:           8
        .value_kind:     global_buffer
      - .address_space:  global
        .offset:         24
        .size:           8
        .value_kind:     global_buffer
      - .address_space:  global
        .offset:         32
        .size:           8
        .value_kind:     global_buffer
      - .offset:         40
        .size:           4
        .value_kind:     hidden_block_count_x
      - .offset:         44
        .size:           4
        .value_kind:     hidden_block_count_y
      - .offset:         48
        .size:           4
        .value_kind:     hidden_block_count_z
      - .offset:         52
        .size:           2
        .value_kind:     hidden_group_size_x
      - .offset:         54
        .size:           2
        .value_kind:     hidden_group_size_y
      - .offset:         56
        .size:           2
        .value_kind:     hidden_group_size_z
      - .offset:         58
        .size:           2
        .value_kind:     hidden_remainder_x
      - .offset:         60
        .size:           2
        .value_kind:     hidden_remainder_y
      - .offset:         62
        .size:           2
        .value_kind:     hidden_remainder_z
      - .offset:         80
        .size:           8
        .value_kind:     hidden_global_offset_x
      - .offset:         88
        .size:           8
        .value_kind:     hidden_global_offset_y
      - .offset:         96
        .size:           8
        .value_kind:     hidden_global_offset_z
      - .offset:         104
        .size:           2
        .value_kind:     hidden_grid_dims
      - .offset:         160
        .size:           4
        .value_kind:     hidden_dynamic_lds_size
    .group_segment_fixed_size: 0
    .kernarg_segment_align: 8
    .kernarg_segment_size: 296
    .language:       OpenCL C
    .language_version:
      - 2
      - 0
    .max_flat_workgroup_size: 512
    .name:           _Z11gemm_8phaseILi0EEvPKDF16_S1_PfPKfS4_
    .private_segment_fixed_size: 0
    .sgpr_count:     59
    .sgpr_spill_count: 0
    .symbol:         _Z11gemm_8phaseILi0EEvPKDF16_S1_PfPKfS4_.kd
    .uniform_work_group_size: 1
    .uses_dynamic_stack: false
    .vgpr_count:     226
    .vgpr_spill_count: 0
    .wavefront_size: 64
  - .agpr_count:     0
    .args:
      - .address_space:  global
        .offset:         0
        .size:           8
        .value_kind:     global_buffer
      - .address_space:  global
        .offset:         8
        .size:           8
        .value_kind:     global_buffer
      - .address_space:  global
        .offset:         16
        .size:           8
        .value_kind:     global_buffer
      - .address_space:  global
        .offset:         24
        .size:           8
        .value_kind:     global_buffer
      - .address_space:  global
        .offset:         32
        .size:           8
        .value_kind:     global_buffer
      - .offset:         40
        .size:           4
        .value_kind:     hidden_block_count_x
      - .offset:         44
        .size:           4
        .value_kind:     hidden_block_count_y
      - .offset:         48
        .size:           4
        .value_kind:     hidden_block_count_z
      - .offset:         52
        .size:           2
        .value_kind:     hidden_group_size_x
      - .offset:         54
        .size:           2
        .value_kind:     hidden_group_size_y
      - .offset:         56
        .size:           2
        .value_kind:     hidden_group_size_z
      - .offset:         58
        .size:           2
        .value_kind:     hidden_remainder_x
      - .offset:         60
        .size:           2
        .value_kind:     hidden_remainder_y
      - .offset:         62
        .size:           2
        .value_kind:     hidden_remainder_z
      - .offset:         80
        .size:           8
        .value_kind:     hidden_global_offset_x
      - .offset:         88
        .size:           8
        .value_kind:     hidden_global_offset_y
      - .offset:         96
        .size:           8
        .value_kind:     hidden_global_offset_z
      - .offset:         104
        .size:           2
        .value_kind:     hidden_grid_dims
      - .offset:         160
        .size:           4
        .value_kind:     hidden_dynamic_lds_size
    .group_segment_fixed_size: 0
    .kernarg_segment_align: 8
    .kernarg_segment_size: 296
    .language:       OpenCL C
    .language_version:
      - 2
      - 0
    .max_flat_workgroup_size: 512
    .name:           _Z11gemm_8phaseILi1EEvPKDF16_S1_PfPKfS4_
    .private_segment_fixed_size: 0
    .sgpr_count:     44
    .sgpr_spill_count: 0
    .symbol:         _Z11gemm_8phaseILi1EEvPKDF16_S1_PfPKfS4_.kd
    .uniform_work_group_size: 1
    .uses_dynamic_stack: false
    .vgpr_count:     234
    .vgpr_spill_count: 0
    .wavefront_size: 64
